# selected attention: row-level select mask via softmax offset (2 cndmask per tile); branch-combine phase: 4 chunks per thread in flight
# speedup vs baseline: 1.0262x; 1.0089x over previous
.LBB0_833:
	ds_read_b128 v[66:69], v217 offset:49152
	ds_read_b128 v[102:105], v217 offset:49280
	v_add_f32_e32 v179, 0, v175
	v_add_f32_e32 v179, v177, v179
	v_add_f32_e32 v179, v173, v179
	s_waitcnt lgkmcnt(1)
	v_mfma_f32_32x32x16_bf16 v[86:101], v[66:69], v[158:161], 0
	ds_read_b128 v[66:69], v217 offset:57344
	ds_read_b128 v[106:109], v217 offset:57472
	v_add_f32_e32 v179, v176, v179
	v_add_f32_e32 v179, v172, v179
	v_add_f32_e32 v179, v174, v179
	v_add_f32_e32 v179, v170, v179
	v_add_f32_e32 v179, v171, v179
	v_add_f32_e32 v179, v165, v179
	s_waitcnt lgkmcnt(1)
	v_mfma_f32_32x32x16_bf16 v[70:85], v[66:69], v[158:161], 0
	ds_read_b128 v[66:69], v218 offset:49152
	ds_read_b128 v[110:113], v218 offset:57344
	ds_read_b128 v[180:183], v218 offset:49280
	v_add_f32_e32 v179, v168, v179
	v_exp_f32_e32 v128, v128
	v_exp_f32_e32 v129, v129
	v_exp_f32_e32 v126, v126
	v_exp_f32_e32 v127, v127
	s_waitcnt lgkmcnt(2)
	v_mfma_f32_32x32x16_bf16 v[86:101], v[66:69], v[154:157], v[86:101]
	ds_read_b128 v[66:69], v218 offset:57472
	ds_read_b128 v[184:187], v219 offset:49152
	ds_read_b128 v[188:191], v219 offset:49280
	ds_read_b128 v[230:233], v219 offset:57344
	ds_read_b128 v[234:237], v219 offset:57472
	ds_read_b128 v[238:241], v220 offset:49152
	ds_read_b128 v[242:245], v220 offset:49280
	v_exp_f32_e32 v124, v124
	v_exp_f32_e32 v125, v125
	v_exp_f32_e32 v122, v122
	v_exp_f32_e32 v123, v123
	v_exp_f32_e32 v120, v120
	v_exp_f32_e32 v121, v121
	s_waitcnt lgkmcnt(8)
	v_mfma_f32_32x32x16_bf16 v[70:85], v[110:113], v[154:157], v[70:85]
	ds_read_b128 v[110:113], v220 offset:57344
	ds_read_b128 v[246:249], v220 offset:57472
	v_exp_f32_e32 v118, v118
	v_exp_f32_e32 v119, v119
	v_exp_f32_e32 v116, v116
	v_exp_f32_e32 v117, v117
	v_exp_f32_e32 v114, v114
	v_exp_f32_e32 v115, v115
	s_waitcnt lgkmcnt(7)
	v_mfma_f32_32x32x16_bf16 v[86:101], v[184:187], v[150:153], v[86:101]
	s_add_i32 s34, s52, s31
	s_add_i32 s8, s34, -2
	s_waitcnt lgkmcnt(5)
	v_mfma_f32_32x32x16_bf16 v[70:85], v[230:233], v[150:153], v[70:85]
	s_waitcnt lgkmcnt(3)
	v_mfma_f32_32x32x16_bf16 v[86:101], v[238:241], v[146:149], v[86:101]
	s_waitcnt lgkmcnt(1)
	v_mfma_f32_32x32x16_bf16 v[70:85], v[110:113], v[146:149], v[70:85]
	v_add_f32_e32 v110, v163, v179
	v_add_f32_e32 v110, v166, v110
	v_add_f32_e32 v110, v162, v110
	v_add_f32_e32 v110, v169, v110
	v_add_f32_e32 v110, v164, v110
	v_add_f32_e32 v110, v167, v110
	v_add_f32_e32 v110, v128, v110
	v_mfma_f32_32x32x16_bf16 v[86:101], v[102:105], v[142:145], v[86:101]
	v_add_f32_e32 v102, v129, v110
	v_add_f32_e32 v102, v126, v102
	v_add_f32_e32 v102, v127, v102
	v_add_f32_e32 v102, v124, v102
	v_add_f32_e32 v102, v125, v102
	v_add_f32_e32 v102, v122, v102
	v_add_f32_e32 v102, v123, v102
	v_mfma_f32_32x32x16_bf16 v[70:85], v[106:109], v[142:145], v[70:85]
	v_add_f32_e32 v102, v120, v102
	v_add_f32_e32 v102, v121, v102
	v_add_f32_e32 v102, v118, v102
	v_add_f32_e32 v102, v119, v102
	v_add_f32_e32 v102, v116, v102
	v_add_f32_e32 v102, v117, v102
	v_add_f32_e32 v102, v114, v102
	v_mfma_f32_32x32x16_bf16 v[86:101], v[180:183], v[138:141], v[86:101]
	v_add_f32_e32 v230, v115, v102
	v_mov_b32_e32 v231, v230
	s_nop 1
	v_permlane32_swap_b32_e32 v230, v231
	v_cvt_pk_bf16_f32 v102, v175, v177
	v_cvt_pk_bf16_f32 v103, v173, v176
	v_cvt_pk_bf16_f32 v104, v172, v174
	v_mfma_f32_32x32x16_bf16 v[70:85], v[66:69], v[138:141], v[70:85]
	v_cvt_pk_bf16_f32 v105, v170, v171
	v_cvt_pk_bf16_f32 v66, v165, v168
	v_cvt_pk_bf16_f32 v67, v163, v166
	v_cvt_pk_bf16_f32 v68, v162, v169
	v_cvt_pk_bf16_f32 v69, v164, v167
	v_cvt_pk_bf16_f32 v106, v128, v129
	v_cvt_pk_bf16_f32 v107, v126, v127
	v_mfma_f32_32x32x16_bf16 v[86:101], v[188:191], v[134:137], v[86:101]
	v_cvt_pk_bf16_f32 v108, v124, v125
	v_cvt_pk_bf16_f32 v109, v122, v123
	v_cvt_pk_bf16_f32 v110, v120, v121
	v_cvt_pk_bf16_f32 v111, v118, v119
	v_cvt_pk_bf16_f32 v112, v116, v117
	v_cvt_pk_bf16_f32 v113, v114, v115
	v_permlane32_swap_b32_e32 v102, v104
	v_mfma_f32_32x32x16_bf16 v[70:85], v[234:237], v[134:137], v[70:85]
	v_permlane32_swap_b32_e32 v103, v105
	v_permlane32_swap_b32_e32 v66, v68
	v_permlane32_swap_b32_e32 v67, v69
	v_permlane32_swap_b32_e32 v106, v108
	v_mfma_f32_32x32x16_bf16 v[86:101], v[242:245], v[130:133], v[86:101]
	v_permlane32_swap_b32_e32 v107, v109
	v_permlane32_swap_b32_e32 v110, v112
	v_permlane32_swap_b32_e32 v111, v113
	s_waitcnt lgkmcnt(0)
	v_mfma_f32_32x32x16_bf16 v[70:85], v[246:249], v[130:133], v[70:85]
	v_add_u32_e32 v236, s30, v195
	v_add_u32_e32 v118, 1, v236
	v_mad_u64_u32 v[114:115], s[0:1], v118, s13, v[206:207]
	v_add_u32_e32 v119, 33, v236
	v_mad_u64_u32 v[116:117], s[0:1], v119, s13, v[206:207]
	global_load_dwordx4 v[162:165], v[114:115], off
	global_load_dwordx4 v[166:169], v[116:117], off
	v_mad_u64_u32 v[114:115], s[0:1], v118, s13, v[208:209]
	v_mad_u64_u32 v[116:117], s[0:1], v119, s13, v[208:209]
	global_load_dwordx4 v[170:173], v[114:115], off
	global_load_dwordx4 v[174:177], v[116:117], off
	ds_read_b64_tr_b16 v[114:115], v212 offset:0
	ds_read_b64_tr_b16 v[116:117], v212 offset:0x800
	ds_read_b64_tr_b16 v[118:119], v212 offset:0x1000
	ds_read_b64_tr_b16 v[120:121], v212 offset:0x1800
	ds_read_b64_tr_b16 v[122:123], v212 offset:0x2000
	ds_read_b64_tr_b16 v[124:125], v212 offset:0x2800
	ds_read_b64_tr_b16 v[126:127], v212 offset:0x3000
	ds_read_b64_tr_b16 v[128:129], v212 offset:0x3800
	s_waitcnt lgkmcnt(0)
	s_nop 0
	v_mfma_f32_32x32x16_bf16 v[50:65], v[102:105], v[114:117], v[50:65]
	ds_read_b64_tr_b16 v[114:115], v212 offset:0x200
	ds_read_b64_tr_b16 v[116:117], v212 offset:0xa00
	v_mfma_f32_32x32x16_bf16 v[50:65], v[66:69], v[118:121], v[50:65]
	ds_read_b64_tr_b16 v[118:119], v212 offset:0x1200
	ds_read_b64_tr_b16 v[120:121], v212 offset:0x1a00
	v_mfma_f32_32x32x16_bf16 v[50:65], v[106:109], v[122:125], v[50:65]
	ds_read_b64_tr_b16 v[122:123], v212 offset:0x2200
	ds_read_b64_tr_b16 v[124:125], v212 offset:0x2a00
	ds_read_b64_tr_b16 v[180:181], v212 offset:0x3200
	ds_read_b64_tr_b16 v[182:183], v212 offset:0x3a00
	s_waitcnt lgkmcnt(0)
	v_mfma_f32_32x32x16_bf16 v[50:65], v[110:113], v[126:129], v[50:65]
	v_mfma_f32_32x32x16_bf16 v[34:49], v[102:105], v[114:117], v[34:49]
	ds_read_b64_tr_b16 v[114:115], v212 offset:0x400
	ds_read_b64_tr_b16 v[116:117], v212 offset:0xc00
	v_mfma_f32_32x32x16_bf16 v[34:49], v[66:69], v[118:121], v[34:49]
	ds_read_b64_tr_b16 v[118:119], v212 offset:0x1400
	ds_read_b64_tr_b16 v[120:121], v212 offset:0x1c00
	v_mfma_f32_32x32x16_bf16 v[34:49], v[106:109], v[122:125], v[34:49]
	ds_read_b64_tr_b16 v[122:123], v212 offset:0x2400
	ds_read_b64_tr_b16 v[124:125], v212 offset:0x2c00
	ds_read_b64_tr_b16 v[126:127], v212 offset:0x3400
	ds_read_b64_tr_b16 v[128:129], v212 offset:0x3c00
	s_waitcnt lgkmcnt(0)
	v_mfma_f32_32x32x16_bf16 v[34:49], v[110:113], v[180:183], v[34:49]
	v_mfma_f32_32x32x16_bf16 v[18:33], v[102:105], v[114:117], v[18:33]
	ds_read_b64_tr_b16 v[114:115], v212 offset:0x600
	ds_read_b64_tr_b16 v[116:117], v212 offset:0xe00
	v_mfma_f32_32x32x16_bf16 v[18:33], v[66:69], v[118:121], v[18:33]
	ds_read_b64_tr_b16 v[118:119], v212 offset:0x1600
	ds_read_b64_tr_b16 v[120:121], v212 offset:0x1e00
	v_mfma_f32_32x32x16_bf16 v[18:33], v[106:109], v[122:125], v[18:33]
	ds_read_b64_tr_b16 v[122:123], v212 offset:0x2600
	ds_read_b64_tr_b16 v[124:125], v212 offset:0x2e00
	ds_read_b64_tr_b16 v[180:181], v212 offset:0x3600
	ds_read_b64_tr_b16 v[182:183], v212 offset:0x3e00
	s_waitcnt lgkmcnt(0)
	v_mfma_f32_32x32x16_bf16 v[18:33], v[110:113], v[126:129], v[18:33]
	v_mfma_f32_32x32x16_bf16 v[2:17], v[102:105], v[114:117], v[2:17]
	s_lshl_b32 s0, 1, s8
	v_mfma_f32_32x32x16_bf16 v[2:17], v[66:69], v[118:121], v[2:17]
	v_and_b32_e32 v66, s0, v225
	v_cmp_eq_u32_e32 vcc, 0, v66
	s_cmp_lg_u64 vcc, 0
	s_cselect_b64 s[0:1], -1, 0
	s_cmp_gt_i32 s30, s49
	s_cselect_b64 s[2:3], -1, 0
	s_mov_b64 s[0:1], s[2:3]
	v_mfma_f32_32x32x16_bf16 v[2:17], v[106:109], v[122:125], v[2:17]
	v_cmp_ne_u32_e64 s[8:9], 0, v66
	v_cmp_ne_u32_e64 s[100:101], 0, v66
	s_andn2_b64 vcc, exec, s[0:1]
	v_mfma_f32_32x32x16_bf16 v[2:17], v[110:113], v[180:183], v[2:17]
	s_cbranch_vccnz .LBB0_835
	v_add_u32_e32 v66, 64, v229
	v_cmp_lt_i32_e32 vcc, -1, v66
	s_and_b64 vcc, s[8:9], vcc
	s_nop 0
	v_cndmask_b32_e32 v86, v221, v86, vcc
	v_cmp_lt_i32_e32 vcc, 31, v66
	s_and_b64 vcc, s[8:9], vcc
	s_nop 0
	v_cndmask_b32_e32 v70, v221, v70, vcc
	v_cmp_lt_i32_e32 vcc, 0, v66
	s_and_b64 vcc, s[8:9], vcc
	s_nop 0
	v_cndmask_b32_e32 v87, v221, v87, vcc
	v_cmp_lt_i32_e32 vcc, 32, v66
	s_and_b64 vcc, s[8:9], vcc
	s_nop 0
	v_cndmask_b32_e32 v71, v221, v71, vcc
	v_cmp_lt_i32_e32 vcc, 1, v66
	s_and_b64 vcc, s[8:9], vcc
	s_nop 0
	v_cndmask_b32_e32 v88, v221, v88, vcc
	v_cmp_lt_i32_e32 vcc, 33, v66
	s_and_b64 vcc, s[8:9], vcc
	s_nop 0
	v_cndmask_b32_e32 v72, v221, v72, vcc
	v_cmp_lt_i32_e32 vcc, 2, v66
	s_and_b64 vcc, s[8:9], vcc
	s_nop 0
	v_cndmask_b32_e32 v89, v221, v89, vcc
	v_cmp_lt_i32_e32 vcc, 34, v66
	s_and_b64 vcc, s[8:9], vcc
	s_nop 0
	v_cndmask_b32_e32 v73, v221, v73, vcc
	v_cmp_lt_i32_e32 vcc, 7, v66
	s_and_b64 vcc, s[8:9], vcc
	s_nop 0
	v_cndmask_b32_e32 v90, v221, v90, vcc
	v_cmp_lt_i32_e32 vcc, 39, v66
	s_and_b64 vcc, s[8:9], vcc
	s_nop 0
	v_cndmask_b32_e32 v74, v221, v74, vcc
	v_cmp_lt_i32_e32 vcc, 8, v66
	s_and_b64 vcc, s[8:9], vcc
	s_nop 0
	v_cndmask_b32_e32 v91, v221, v91, vcc
	v_cmp_lt_i32_e32 vcc, 40, v66
	s_and_b64 vcc, s[8:9], vcc
	s_nop 0
	v_cndmask_b32_e32 v75, v221, v75, vcc
	v_cmp_lt_i32_e32 vcc, 9, v66
	s_and_b64 vcc, s[8:9], vcc
	s_nop 0
	v_cndmask_b32_e32 v92, v221, v92, vcc
	v_cmp_lt_i32_e32 vcc, 41, v66
	s_and_b64 vcc, s[8:9], vcc
	s_nop 0
	v_cndmask_b32_e32 v76, v221, v76, vcc
	v_cmp_lt_i32_e32 vcc, 10, v66
	s_and_b64 vcc, s[8:9], vcc
	s_nop 0
	v_cndmask_b32_e32 v93, v221, v93, vcc
	v_cmp_lt_i32_e32 vcc, 42, v66
	s_and_b64 vcc, s[8:9], vcc
	s_nop 0
	v_cndmask_b32_e32 v77, v221, v77, vcc
	v_cmp_lt_i32_e32 vcc, 15, v66
	s_and_b64 vcc, s[8:9], vcc
	s_nop 0
	v_cndmask_b32_e32 v94, v221, v94, vcc
	v_cmp_lt_i32_e32 vcc, 47, v66
	s_and_b64 vcc, s[8:9], vcc
	s_nop 0
	v_cndmask_b32_e32 v78, v221, v78, vcc
	v_cmp_lt_i32_e32 vcc, 16, v66
	s_and_b64 vcc, s[8:9], vcc
	s_nop 0
	v_cndmask_b32_e32 v95, v221, v95, vcc
	v_cmp_lt_i32_e32 vcc, 48, v66
	s_and_b64 vcc, s[8:9], vcc
	s_nop 0
	v_cndmask_b32_e32 v79, v221, v79, vcc
	v_cmp_lt_i32_e32 vcc, 17, v66
	s_and_b64 vcc, s[8:9], vcc
	s_nop 0
	v_cndmask_b32_e32 v96, v221, v96, vcc
	v_cmp_lt_i32_e32 vcc, 49, v66
	s_and_b64 vcc, s[8:9], vcc
	s_nop 0
	v_cndmask_b32_e32 v80, v221, v80, vcc
	v_cmp_lt_i32_e32 vcc, 18, v66
	s_and_b64 vcc, s[8:9], vcc
	s_nop 0
	v_cndmask_b32_e32 v97, v221, v97, vcc
	v_cmp_lt_i32_e32 vcc, 50, v66
	s_and_b64 vcc, s[8:9], vcc
	s_nop 0
	v_cndmask_b32_e32 v81, v221, v81, vcc
	v_cmp_lt_i32_e32 vcc, 23, v66
	s_and_b64 vcc, s[8:9], vcc
	s_nop 0
	v_cndmask_b32_e32 v98, v221, v98, vcc
	v_cmp_lt_i32_e32 vcc, 55, v66
	s_and_b64 vcc, s[8:9], vcc
	s_nop 0
	v_cndmask_b32_e32 v82, v221, v82, vcc
	v_cmp_lt_i32_e32 vcc, 24, v66
	s_and_b64 vcc, s[8:9], vcc
	s_nop 0
	v_cndmask_b32_e32 v99, v221, v99, vcc
	v_cmp_lt_i32_e32 vcc, 56, v66
	s_and_b64 vcc, s[8:9], vcc
	s_nop 0
	v_cndmask_b32_e32 v83, v221, v83, vcc
	v_cmp_lt_i32_e32 vcc, 25, v66
	s_and_b64 vcc, s[8:9], vcc
	s_nop 0
	v_cndmask_b32_e32 v100, v221, v100, vcc
	v_cmp_lt_i32_e32 vcc, 57, v66
	s_and_b64 vcc, s[8:9], vcc
	s_nop 0
	v_cndmask_b32_e32 v84, v221, v84, vcc
	v_cmp_lt_i32_e32 vcc, 26, v66
	s_and_b64 vcc, s[8:9], vcc
	s_nop 0
	v_cndmask_b32_e32 v101, v221, v101, vcc
	v_cmp_lt_i32_e32 vcc, 58, v66
	s_and_b64 vcc, s[8:9], vcc
	s_nop 0
	v_cndmask_b32_e32 v85, v221, v85, vcc
.LBB0_835:
	v_max_f32_e32 v66, v87, v87
	v_max_f32_e32 v67, v86, v86
	v_max_f32_e32 v66, v67, v66
	v_max3_f32 v66, v66, v88, v89
	v_max3_f32 v66, v66, v90, v91
	v_max3_f32 v66, v66, v92, v93
	v_max3_f32 v66, v66, v94, v95
	v_max3_f32 v66, v66, v96, v97
	v_max3_f32 v66, v66, v98, v99
	v_max3_f32 v66, v66, v100, v101
	v_max3_f32 v66, v66, v70, v71
	v_max3_f32 v66, v66, v72, v73
	v_max3_f32 v66, v66, v74, v75
	v_max3_f32 v66, v66, v76, v77
	v_max3_f32 v66, v66, v78, v79
	v_max3_f32 v66, v66, v80, v81
	v_max3_f32 v66, v66, v82, v83
	v_max3_f32 v66, v66, v84, v85
	v_mov_b32_e32 v67, v66
	s_nop 1
	v_permlane32_swap_b32_e32 v66, v67
	v_max_f32_e32 v67, v67, v67
	v_max_f32_e32 v66, v66, v66
	v_max_f32_e32 v66, v66, v67
	v_cndmask_b32_e64 v66, v221, v66, s[100:101]
	v_max_f32_e32 v68, v178, v178
	v_sub_f32_e32 v67, v66, v178
	v_max_f32_e32 v66, v68, v66
	v_sub_f32_e32 v68, v178, v66
	v_mul_f32_e32 v68, 0x3e0293ee, v68
	v_mul_f32_e32 v67, 0x3db504f3, v67
	v_exp_f32_e32 v68, v68
	v_cmp_ge_f32_e32 vcc, s44, v67
	s_cmp_eq_u64 vcc, exec
	s_cselect_b64 s[8:9], -1, 0
	s_barrier
	s_waitcnt vmcnt(0)
	v_cndmask_b32_e64 v232, v68, 1.0, s[8:9]
	v_cmp_gt_f32_e32 vcc, 1.0, v232
	s_waitcnt vmcnt(3)
	ds_write_b128 v215, v[162:165]
	s_waitcnt vmcnt(2)
	ds_write_b128 v216, v[166:169]
	s_waitcnt vmcnt(1)
	ds_write_b128 v222, v[170:173] offset:32768
	s_waitcnt vmcnt(0)
	ds_write_b128 v222, v[174:177] offset:40960
	s_cbranch_vccz .LBB0_839
	s_and_saveexec_b64 s[28:29], s[4:5]
	ds_write_b32 v224, v232 offset:128
	s_or_b64 exec, exec, s[28:29]
	s_waitcnt lgkmcnt(0)
	ds_read_b128 v[102:105], v205 offset:224
	ds_read_b128 v[106:109], v205 offset:192
	ds_read_b128 v[110:113], v205 offset:160
	ds_read_b128 v[114:117], v205 offset:128
	s_waitcnt lgkmcnt(3)
	v_pk_mul_f32 v[64:65], v[64:65], v[104:105]
	s_waitcnt lgkmcnt(2)
	v_pk_mul_f32 v[60:61], v[60:61], v[108:109]
	s_waitcnt lgkmcnt(1)
	v_pk_mul_f32 v[56:57], v[56:57], v[112:113]
	s_waitcnt lgkmcnt(0)
	v_pk_mul_f32 v[52:53], v[52:53], v[116:117]
	v_pk_mul_f32 v[62:63], v[62:63], v[102:103]
	v_pk_mul_f32 v[58:59], v[58:59], v[106:107]
	v_pk_mul_f32 v[54:55], v[54:55], v[110:111]
	v_pk_mul_f32 v[50:51], v[50:51], v[114:115]
	v_pk_mul_f32 v[48:49], v[48:49], v[104:105]
	v_pk_mul_f32 v[44:45], v[44:45], v[108:109]
	v_pk_mul_f32 v[40:41], v[40:41], v[112:113]
	v_pk_mul_f32 v[36:37], v[36:37], v[116:117]
	v_pk_mul_f32 v[46:47], v[46:47], v[102:103]
	v_pk_mul_f32 v[42:43], v[42:43], v[106:107]
	v_pk_mul_f32 v[38:39], v[38:39], v[110:111]
	v_pk_mul_f32 v[34:35], v[34:35], v[114:115]
	v_pk_mul_f32 v[32:33], v[32:33], v[104:105]
	v_pk_mul_f32 v[28:29], v[28:29], v[108:109]
	v_pk_mul_f32 v[24:25], v[24:25], v[112:113]
	v_pk_mul_f32 v[20:21], v[20:21], v[116:117]
	v_pk_mul_f32 v[30:31], v[30:31], v[102:103]
	v_pk_mul_f32 v[26:27], v[26:27], v[106:107]
	v_pk_mul_f32 v[22:23], v[22:23], v[110:111]
	v_pk_mul_f32 v[18:19], v[18:19], v[114:115]
	v_pk_mul_f32 v[16:17], v[16:17], v[104:105]
	v_pk_mul_f32 v[12:13], v[12:13], v[108:109]
	v_pk_mul_f32 v[8:9], v[8:9], v[112:113]
	v_pk_mul_f32 v[4:5], v[4:5], v[116:117]
	v_pk_mul_f32 v[14:15], v[14:15], v[102:103]
	v_pk_mul_f32 v[10:11], v[10:11], v[106:107]
	v_pk_mul_f32 v[6:7], v[6:7], v[110:111]
	v_pk_mul_f32 v[2:3], v[2:3], v[114:115]
.LBB0_839:
	v_cndmask_b32_e64 v233, v66, v178, s[8:9]
	v_mul_f32_e32 v178, 0xbe0293ee, v233
	v_cndmask_b32_e64 v178, v221, v178, s[100:101]
	v_fmamk_f32 v66, v86, 0x3e0293ee, v178
	v_fmamk_f32 v67, v87, 0x3e0293ee, v178
	v_fmamk_f32 v68, v88, 0x3e0293ee, v178
	v_fmamk_f32 v69, v89, 0x3e0293ee, v178
	v_fmamk_f32 v102, v90, 0x3e0293ee, v178
	v_fmamk_f32 v103, v91, 0x3e0293ee, v178
	v_fmamk_f32 v104, v92, 0x3e0293ee, v178
	v_fmamk_f32 v105, v93, 0x3e0293ee, v178
	v_fmamk_f32 v106, v94, 0x3e0293ee, v178
	v_fmamk_f32 v107, v95, 0x3e0293ee, v178
	v_fmamk_f32 v108, v96, 0x3e0293ee, v178
	v_fmamk_f32 v109, v97, 0x3e0293ee, v178
	v_fmamk_f32 v98, v98, 0x3e0293ee, v178
	v_fmamk_f32 v99, v99, 0x3e0293ee, v178
	v_fmamk_f32 v100, v100, 0x3e0293ee, v178
	v_fmamk_f32 v101, v101, 0x3e0293ee, v178
	v_fmamk_f32 v86, v70, 0x3e0293ee, v178
	v_fmamk_f32 v95, v71, 0x3e0293ee, v178
	v_fmamk_f32 v96, v72, 0x3e0293ee, v178
	v_fmamk_f32 v97, v73, 0x3e0293ee, v178
	v_fmamk_f32 v179, v74, 0x3e0293ee, v178
	v_fmamk_f32 v87, v75, 0x3e0293ee, v178
	v_fmamk_f32 v88, v76, 0x3e0293ee, v178
	v_fmamk_f32 v89, v77, 0x3e0293ee, v178
	v_fmamk_f32 v90, v78, 0x3e0293ee, v178
	v_fmamk_f32 v91, v79, 0x3e0293ee, v178
	v_fmamk_f32 v92, v80, 0x3e0293ee, v178
	v_fmamk_f32 v93, v81, 0x3e0293ee, v178
	v_exp_f32_e32 v66, v66
	v_exp_f32_e32 v67, v67
	v_exp_f32_e32 v68, v68
	v_exp_f32_e32 v69, v69
	v_exp_f32_e32 v70, v102
	v_exp_f32_e32 v71, v103
	v_exp_f32_e32 v72, v104
	v_exp_f32_e32 v73, v105
	v_exp_f32_e32 v74, v106
	v_exp_f32_e32 v75, v107
	v_exp_f32_e32 v76, v108
	v_exp_f32_e32 v77, v109
	v_exp_f32_e32 v78, v98
	v_exp_f32_e32 v79, v99
	v_exp_f32_e32 v80, v100
	v_exp_f32_e32 v81, v101
	v_fmamk_f32 v94, v82, 0x3e0293ee, v178
	v_fmamk_f32 v180, v83, 0x3e0293ee, v178
	v_fmamk_f32 v181, v84, 0x3e0293ee, v178
	v_fmac_f32_e32 v178, 0x3e0293ee, v85
	s_waitcnt lgkmcnt(0)
	s_barrier
	ds_read_b128 v[82:85], v217 offset:32768
	ds_read_b128 v[98:101], v217 offset:40960
	v_exp_f32_e32 v87, v87
	v_exp_f32_e32 v88, v88
	v_exp_f32_e32 v89, v89
	s_waitcnt lgkmcnt(1)
	v_mfma_f32_32x32x16_bf16 v[114:129], v[82:85], v[158:161], 0
	ds_read_b128 v[82:85], v218 offset:32768
	ds_read_b128 v[182:185], v218 offset:40960
	v_exp_f32_e32 v90, v90
	v_exp_f32_e32 v91, v91
	v_exp_f32_e32 v92, v92
	v_exp_f32_e32 v93, v93
	v_exp_f32_e32 v94, v94
	s_waitcnt lgkmcnt(2)
	v_mfma_f32_32x32x16_bf16 v[98:113], v[98:101], v[158:161], 0
	s_waitcnt lgkmcnt(1)
	v_mfma_f32_32x32x16_bf16 v[114:129], v[82:85], v[154:157], v[114:129]
	s_waitcnt lgkmcnt(0)
	v_mfma_f32_32x32x16_bf16 v[98:113], v[182:185], v[154:157], v[98:113]
	ds_read_b128 v[82:85], v219 offset:32768
	ds_read_b128 v[182:185], v219 offset:40960
	s_waitcnt lgkmcnt(1)
	v_mfma_f32_32x32x16_bf16 v[114:129], v[82:85], v[150:153], v[114:129]
	s_waitcnt lgkmcnt(0)
	v_mfma_f32_32x32x16_bf16 v[98:113], v[182:185], v[150:153], v[98:113]
	ds_read_b128 v[82:85], v220 offset:32768
	ds_read_b128 v[182:185], v220 offset:40960
	s_waitcnt lgkmcnt(1)
	v_mfma_f32_32x32x16_bf16 v[114:129], v[82:85], v[146:149], v[114:129]
	s_waitcnt lgkmcnt(0)
	v_mfma_f32_32x32x16_bf16 v[98:113], v[182:185], v[146:149], v[98:113]
	ds_read_b128 v[82:85], v217 offset:32896
	ds_read_b128 v[182:185], v217 offset:41088
	s_waitcnt lgkmcnt(1)
	v_mfma_f32_32x32x16_bf16 v[114:129], v[82:85], v[142:145], v[114:129]
	s_waitcnt lgkmcnt(0)
	v_mfma_f32_32x32x16_bf16 v[98:113], v[182:185], v[142:145], v[98:113]
	ds_read_b128 v[82:85], v218 offset:32896
	ds_read_b128 v[182:185], v218 offset:41088
	s_waitcnt lgkmcnt(1)
	v_mfma_f32_32x32x16_bf16 v[114:129], v[82:85], v[138:141], v[114:129]
	s_waitcnt lgkmcnt(0)
	v_mfma_f32_32x32x16_bf16 v[98:113], v[182:185], v[138:141], v[98:113]
	ds_read_b128 v[82:85], v219 offset:32896
	ds_read_b128 v[182:185], v219 offset:41088
	s_waitcnt lgkmcnt(1)
	v_mfma_f32_32x32x16_bf16 v[114:129], v[82:85], v[134:137], v[114:129]
	s_waitcnt lgkmcnt(0)
	v_mfma_f32_32x32x16_bf16 v[98:113], v[182:185], v[134:137], v[98:113]
	ds_read_b128 v[82:85], v220 offset:32896
	ds_read_b128 v[182:185], v220 offset:41088
	s_waitcnt lgkmcnt(1)
	v_mfma_f32_32x32x16_bf16 v[114:129], v[82:85], v[130:133], v[114:129]
	v_exp_f32_e32 v85, v97
	v_exp_f32_e32 v97, v178
	v_add_f32_e32 v178, 0, v66
	v_add_f32_e32 v178, v67, v178
	v_add_f32_e32 v178, v68, v178
	v_add_f32_e32 v178, v69, v178
	v_add_f32_e32 v178, v70, v178
	v_add_f32_e32 v178, v71, v178
	v_add_f32_e32 v178, v72, v178
	v_add_f32_e32 v178, v73, v178
	v_add_f32_e32 v178, v74, v178
	v_add_f32_e32 v178, v75, v178
	v_add_f32_e32 v178, v76, v178
	v_add_f32_e32 v178, v77, v178
	v_exp_f32_e32 v82, v86
	v_add_f32_e32 v178, v78, v178
	v_exp_f32_e32 v83, v95
	v_add_f32_e32 v178, v79, v178
	v_exp_f32_e32 v84, v96
	v_add_f32_e32 v178, v80, v178
	v_add_f32_e32 v178, v81, v178
	v_exp_f32_e32 v86, v179
	v_add_f32_e32 v178, v82, v178
	v_add_f32_e32 v178, v83, v178
	v_add_f32_e32 v178, v84, v178
	v_add_f32_e32 v178, v85, v178
	v_add_f32_e32 v178, v86, v178
	v_add_f32_e32 v178, v87, v178
	v_add_f32_e32 v178, v88, v178
	v_add_f32_e32 v178, v89, v178
	v_add_f32_e32 v178, v90, v178
	v_exp_f32_e32 v95, v180
	v_add_f32_e32 v178, v91, v178
	s_waitcnt lgkmcnt(0)
	v_mfma_f32_32x32x16_bf16 v[98:113], v[182:185], v[130:133], v[98:113]
	v_exp_f32_e32 v96, v181
	v_add_f32_e32 v178, v92, v178
	v_add_f32_e32 v178, v93, v178
	v_add_f32_e32 v178, v94, v178
	v_add_f32_e32 v178, v95, v178
	v_add_f32_e32 v178, v96, v178
	v_add_f32_e32 v234, v97, v178
	v_mov_b32_e32 v235, v234
	v_cvt_pk_bf16_f32 v178, v66, v67
	v_cvt_pk_bf16_f32 v179, v68, v69
	v_cvt_pk_bf16_f32 v180, v70, v71
	v_cvt_pk_bf16_f32 v181, v72, v73
	v_cvt_pk_bf16_f32 v182, v74, v75
	v_cvt_pk_bf16_f32 v183, v76, v77
	v_cvt_pk_bf16_f32 v184, v78, v79
	v_cvt_pk_bf16_f32 v185, v80, v81
	v_cvt_pk_bf16_f32 v186, v82, v83
	v_cvt_pk_bf16_f32 v187, v84, v85
	v_cvt_pk_bf16_f32 v188, v86, v87
	v_cvt_pk_bf16_f32 v189, v88, v89
	v_cvt_pk_bf16_f32 v190, v90, v91
	v_cvt_pk_bf16_f32 v191, v92, v93
	v_cvt_pk_bf16_f32 v192, v94, v95
	v_cvt_pk_bf16_f32 v193, v96, v97
	s_nop 1
	v_permlane32_swap_b32_e32 v234, v235
	v_permlane32_swap_b32_e32 v178, v180
	v_permlane32_swap_b32_e32 v179, v181
	v_permlane32_swap_b32_e32 v182, v184
	v_permlane32_swap_b32_e32 v183, v185
	v_permlane32_swap_b32_e32 v186, v188
	v_permlane32_swap_b32_e32 v187, v189
	v_permlane32_swap_b32_e32 v190, v192
	v_permlane32_swap_b32_e32 v191, v193
	s_cmp_lt_i32 s31, s51
	s_cselect_b64 s[28:29], -1, 0
	s_cmp_ge_i32 s31, s51
	s_cbranch_scc1 .LBB0_841
	v_add_u32_e32 v170, 0x41, v236
	v_add_u32_e32 v172, 0x61, v236
	v_mad_u64_u32 v[162:163], s[0:1], v170, s13, v[206:207]
	v_mad_u64_u32 v[166:167], s[0:1], v172, s13, v[206:207]
	v_mad_u64_u32 v[170:171], s[0:1], v170, s13, v[208:209]
	v_mad_u64_u32 v[174:175], s[0:1], v172, s13, v[208:209]
	global_load_dwordx4 v[162:165], v[162:163], off
	s_nop 0
	global_load_dwordx4 v[166:169], v[166:167], off
	s_nop 0
	global_load_dwordx4 v[170:173], v[170:171], off
	s_nop 0
	global_load_dwordx4 v[174:177], v[174:175], off
.LBB0_841:
	ds_read_b64_tr_b16 v[236:237], v212 offset:0x4000
	ds_read_b64_tr_b16 v[238:239], v212 offset:0x4800
	ds_read_b64_tr_b16 v[240:241], v212 offset:0x5000
	ds_read_b64_tr_b16 v[242:243], v212 offset:0x5800
	ds_read_b64_tr_b16 v[244:245], v212 offset:0x6000
	ds_read_b64_tr_b16 v[246:247], v212 offset:0x6800
	ds_read_b64_tr_b16 v[248:249], v212 offset:0x7000
	ds_read_b64_tr_b16 v[250:251], v212 offset:0x7800
	s_waitcnt lgkmcnt(0)
	s_add_i32 s2, s30, 64
	s_add_i32 s34, s34, -1
	v_mfma_f32_32x32x16_bf16 v[50:65], v[178:181], v[236:239], v[50:65]
	ds_read_b64_tr_b16 v[236:237], v212 offset:0x4200
	ds_read_b64_tr_b16 v[238:239], v212 offset:0x4a00
	v_mfma_f32_32x32x16_bf16 v[50:65], v[182:185], v[240:243], v[50:65]
	ds_read_b64_tr_b16 v[240:241], v212 offset:0x5200
	ds_read_b64_tr_b16 v[242:243], v212 offset:0x5a00
	v_mfma_f32_32x32x16_bf16 v[50:65], v[186:189], v[244:247], v[50:65]
	ds_read_b64_tr_b16 v[244:245], v212 offset:0x6200
	ds_read_b64_tr_b16 v[246:247], v212 offset:0x6a00
	ds_read_b64_tr_b16 v[198:199], v212 offset:0x7200
	ds_read_b64_tr_b16 v[200:201], v212 offset:0x7a00
	s_waitcnt lgkmcnt(0)
	v_mfma_f32_32x32x16_bf16 v[50:65], v[190:193], v[248:251], v[50:65]
	v_mfma_f32_32x32x16_bf16 v[34:49], v[178:181], v[236:239], v[34:49]
	ds_read_b64_tr_b16 v[236:237], v212 offset:0x4400
	ds_read_b64_tr_b16 v[238:239], v212 offset:0x4c00
	v_mfma_f32_32x32x16_bf16 v[34:49], v[182:185], v[240:243], v[34:49]
	ds_read_b64_tr_b16 v[240:241], v212 offset:0x5400
	ds_read_b64_tr_b16 v[242:243], v212 offset:0x5c00
	v_mfma_f32_32x32x16_bf16 v[34:49], v[186:189], v[244:247], v[34:49]
	ds_read_b64_tr_b16 v[244:245], v212 offset:0x6400
	ds_read_b64_tr_b16 v[246:247], v212 offset:0x6c00
	ds_read_b64_tr_b16 v[248:249], v212 offset:0x7400
	ds_read_b64_tr_b16 v[250:251], v212 offset:0x7c00
	s_waitcnt lgkmcnt(0)
	v_mfma_f32_32x32x16_bf16 v[34:49], v[190:193], v[198:201], v[34:49]
	v_mfma_f32_32x32x16_bf16 v[18:33], v[178:181], v[236:239], v[18:33]
	ds_read_b64_tr_b16 v[198:199], v212 offset:0x4600
	ds_read_b64_tr_b16 v[200:201], v212 offset:0x4e00
	ds_read_b64_tr_b16 v[236:237], v212 offset:0x5600
	ds_read_b64_tr_b16 v[238:239], v212 offset:0x5e00
	v_mfma_f32_32x32x16_bf16 v[18:33], v[182:185], v[240:243], v[18:33]
	ds_read_b64_tr_b16 v[240:241], v212 offset:0x6600
	ds_read_b64_tr_b16 v[242:243], v212 offset:0x6e00
	v_mfma_f32_32x32x16_bf16 v[18:33], v[186:189], v[244:247], v[18:33]
	ds_read_b64_tr_b16 v[244:245], v212 offset:0x7600
	ds_read_b64_tr_b16 v[246:247], v212 offset:0x7e00
	s_waitcnt lgkmcnt(0)
	v_mfma_f32_32x32x16_bf16 v[18:33], v[190:193], v[248:251], v[18:33]
	v_mfma_f32_32x32x16_bf16 v[2:17], v[178:181], v[198:201], v[2:17]
	s_lshl_b32 s0, 1, s34
	v_and_b32_e32 v178, s0, v225
	v_cmp_eq_u32_e32 vcc, 0, v178
	s_cmp_lg_u64 vcc, 0
	s_cselect_b64 s[0:1], -1, 0
	s_cmp_gt_i32 s2, s49
	s_cselect_b64 s[2:3], -1, 0
	v_mfma_f32_32x32x16_bf16 v[2:17], v[182:185], v[236:239], v[2:17]
	s_mov_b64 s[0:1], s[2:3]
	v_cmp_ne_u32_e64 s[8:9], 0, v178
	v_cmp_ne_u32_e64 s[100:101], 0, v178
	s_andn2_b64 vcc, exec, s[0:1]
	v_mfma_f32_32x32x16_bf16 v[2:17], v[186:189], v[240:243], v[2:17]
	v_mfma_f32_32x32x16_bf16 v[2:17], v[190:193], v[244:247], v[2:17]
	s_cbranch_vccnz .LBB0_843
	v_cmp_lt_i32_e32 vcc, -1, v229
	s_and_b64 vcc, s[8:9], vcc
	s_nop 0
	v_cndmask_b32_e32 v114, v221, v114, vcc
	v_cmp_lt_i32_e32 vcc, 31, v229
	s_and_b64 vcc, s[8:9], vcc
	s_nop 0
	v_cndmask_b32_e32 v98, v221, v98, vcc
	v_cmp_lt_i32_e32 vcc, 0, v229
	s_and_b64 vcc, s[8:9], vcc
	s_nop 0
	v_cndmask_b32_e32 v115, v221, v115, vcc
	v_cmp_lt_i32_e32 vcc, 32, v229
	s_and_b64 vcc, s[8:9], vcc
	s_nop 0
	v_cndmask_b32_e32 v99, v221, v99, vcc
	v_cmp_lt_i32_e32 vcc, 1, v229
	s_and_b64 vcc, s[8:9], vcc
	s_nop 0
	v_cndmask_b32_e32 v116, v221, v116, vcc
	v_cmp_lt_i32_e32 vcc, 33, v229
	s_and_b64 vcc, s[8:9], vcc
	s_nop 0
	v_cndmask_b32_e32 v100, v221, v100, vcc
	v_cmp_lt_i32_e32 vcc, 2, v229
	s_and_b64 vcc, s[8:9], vcc
	s_nop 0
	v_cndmask_b32_e32 v117, v221, v117, vcc
	v_cmp_lt_i32_e32 vcc, 34, v229
	s_and_b64 vcc, s[8:9], vcc
	s_nop 0
	v_cndmask_b32_e32 v101, v221, v101, vcc
	v_cmp_lt_i32_e32 vcc, 7, v229
	s_and_b64 vcc, s[8:9], vcc
	s_nop 0
	v_cndmask_b32_e32 v118, v221, v118, vcc
	v_cmp_lt_i32_e32 vcc, 39, v229
	s_and_b64 vcc, s[8:9], vcc
	s_nop 0
	v_cndmask_b32_e32 v102, v221, v102, vcc
	v_cmp_lt_i32_e32 vcc, 8, v229
	s_and_b64 vcc, s[8:9], vcc
	s_nop 0
	v_cndmask_b32_e32 v119, v221, v119, vcc
	v_cmp_lt_i32_e32 vcc, 40, v229
	s_and_b64 vcc, s[8:9], vcc
	s_nop 0
	v_cndmask_b32_e32 v103, v221, v103, vcc
	v_cmp_lt_i32_e32 vcc, 9, v229
	s_and_b64 vcc, s[8:9], vcc
	s_nop 0
	v_cndmask_b32_e32 v120, v221, v120, vcc
	v_cmp_lt_i32_e32 vcc, 41, v229
	s_and_b64 vcc, s[8:9], vcc
	s_nop 0
	v_cndmask_b32_e32 v104, v221, v104, vcc
	v_cmp_lt_i32_e32 vcc, 10, v229
	s_and_b64 vcc, s[8:9], vcc
	s_nop 0
	v_cndmask_b32_e32 v121, v221, v121, vcc
	v_cmp_lt_i32_e32 vcc, 42, v229
	s_and_b64 vcc, s[8:9], vcc
	s_nop 0
	v_cndmask_b32_e32 v105, v221, v105, vcc
	v_cmp_lt_i32_e32 vcc, 15, v229
	s_and_b64 vcc, s[8:9], vcc
	s_nop 0
	v_cndmask_b32_e32 v122, v221, v122, vcc
	v_cmp_lt_i32_e32 vcc, 47, v229
	s_and_b64 vcc, s[8:9], vcc
	s_nop 0
	v_cndmask_b32_e32 v106, v221, v106, vcc
	v_cmp_lt_i32_e32 vcc, 16, v229
	s_and_b64 vcc, s[8:9], vcc
	s_nop 0
	v_cndmask_b32_e32 v123, v221, v123, vcc
	v_cmp_lt_i32_e32 vcc, 48, v229
	s_and_b64 vcc, s[8:9], vcc
	s_nop 0
	v_cndmask_b32_e32 v107, v221, v107, vcc
	v_cmp_lt_i32_e32 vcc, 17, v229
	s_and_b64 vcc, s[8:9], vcc
	s_nop 0
	v_cndmask_b32_e32 v124, v221, v124, vcc
	v_cmp_lt_i32_e32 vcc, 49, v229
	s_and_b64 vcc, s[8:9], vcc
	s_nop 0
	v_cndmask_b32_e32 v108, v221, v108, vcc
	v_cmp_lt_i32_e32 vcc, 18, v229
	s_and_b64 vcc, s[8:9], vcc
	s_nop 0
	v_cndmask_b32_e32 v125, v221, v125, vcc
	v_cmp_lt_i32_e32 vcc, 50, v229
	s_and_b64 vcc, s[8:9], vcc
	s_nop 0
	v_cndmask_b32_e32 v109, v221, v109, vcc
	v_cmp_lt_i32_e32 vcc, 23, v229
	s_and_b64 vcc, s[8:9], vcc
	s_nop 0
	v_cndmask_b32_e32 v126, v221, v126, vcc
	v_cmp_lt_i32_e32 vcc, 55, v229
	s_and_b64 vcc, s[8:9], vcc
	s_nop 0
	v_cndmask_b32_e32 v110, v221, v110, vcc
	v_cmp_lt_i32_e32 vcc, 24, v229
	s_and_b64 vcc, s[8:9], vcc
	s_nop 0
	v_cndmask_b32_e32 v127, v221, v127, vcc
	v_cmp_lt_i32_e32 vcc, 56, v229
	s_and_b64 vcc, s[8:9], vcc
	s_nop 0
	v_cndmask_b32_e32 v111, v221, v111, vcc
	v_cmp_lt_i32_e32 vcc, 25, v229
	s_and_b64 vcc, s[8:9], vcc
	s_nop 0
	v_cndmask_b32_e32 v128, v221, v128, vcc
	v_cmp_lt_i32_e32 vcc, 57, v229
	s_and_b64 vcc, s[8:9], vcc
	s_nop 0
	v_cndmask_b32_e32 v112, v221, v112, vcc
	v_cmp_lt_i32_e32 vcc, 26, v229
	s_and_b64 vcc, s[8:9], vcc
	s_nop 0
	v_cndmask_b32_e32 v129, v221, v129, vcc
	v_cmp_lt_i32_e32 vcc, 58, v229
	s_and_b64 vcc, s[8:9], vcc
	s_nop 0
	v_cndmask_b32_e32 v113, v221, v113, vcc
.LBB0_843:
	v_max_f32_e32 v178, v115, v115
	v_max_f32_e32 v179, v114, v114
	v_max_f32_e32 v178, v179, v178
	v_max3_f32 v178, v178, v116, v117
	v_max3_f32 v178, v178, v118, v119
	v_max3_f32 v178, v178, v120, v121
	v_max3_f32 v178, v178, v122, v123
	v_max3_f32 v178, v178, v124, v125
	v_max3_f32 v178, v178, v126, v127
	v_max3_f32 v178, v178, v128, v129
	v_max3_f32 v178, v178, v98, v99
	v_max3_f32 v178, v178, v100, v101
	v_max3_f32 v178, v178, v102, v103
	v_max3_f32 v178, v178, v104, v105
	v_max3_f32 v178, v178, v106, v107
	v_max3_f32 v178, v178, v108, v109
	v_max3_f32 v178, v178, v110, v111
	v_max3_f32 v178, v178, v112, v113
	v_mov_b32_e32 v179, v178
	s_nop 1
	v_permlane32_swap_b32_e32 v178, v179
	v_max_f32_e32 v179, v179, v179
	v_max_f32_e32 v178, v178, v178
	v_max_f32_e32 v178, v178, v179
	v_cndmask_b32_e64 v178, v221, v178, s[100:101]
	v_sub_f32_e32 v179, v178, v233
	v_mul_f32_e32 v179, 0x3db504f3, v179
	v_cmp_ge_f32_e32 vcc, s44, v179
	s_cmp_eq_u64 vcc, exec
	s_cselect_b64 s[8:9], -1, 0
	s_andn2_b64 vcc, exec, s[28:29]
	s_barrier
	s_cbranch_vccnz .LBB0_845
	s_waitcnt vmcnt(0)
	s_waitcnt vmcnt(3)
	ds_write_b128 v215, v[162:165] offset:16384
	s_waitcnt vmcnt(2)
	ds_write_b128 v216, v[166:169] offset:16384
	s_waitcnt vmcnt(1)
	ds_write_b128 v222, v[170:173] offset:49152
	s_waitcnt vmcnt(0)
	ds_write_b128 v222, v[174:177] offset:57344

.LBB0_849:
	v_cndmask_b32_e64 v178, v162, v233, s[8:9]
	v_mul_f32_e32 v180, 0xbe0293ee, v178
	v_cndmask_b32_e64 v180, v221, v180, s[100:101]
	v_mov_b32_e32 v183, v180
	v_fmamk_f32 v162, v114, 0x3e0293ee, v180
	v_fmamk_f32 v163, v115, 0x3e0293ee, v180
	v_fmamk_f32 v164, v116, 0x3e0293ee, v180
	v_fmamk_f32 v165, v117, 0x3e0293ee, v180
	s_waitcnt vmcnt(2)
	v_fmamk_f32 v166, v118, 0x3e0293ee, v180
	v_fmamk_f32 v167, v119, 0x3e0293ee, v180
	v_fmamk_f32 v168, v120, 0x3e0293ee, v180
	v_fmamk_f32 v169, v121, 0x3e0293ee, v180
	v_fmamk_f32 v181, v122, 0x3e0293ee, v180
	v_fmamk_f32 v182, v123, 0x3e0293ee, v180
	v_fmamk_f32 v124, v124, 0x3e0293ee, v180
	v_fmamk_f32 v125, v125, 0x3e0293ee, v180
	v_fmamk_f32 v126, v126, 0x3e0293ee, v180
	v_fmamk_f32 v127, v127, 0x3e0293ee, v180
	v_fmamk_f32 v128, v128, 0x3e0293ee, v180
	v_fmac_f32_e32 v183, 0x3e0293ee, v129
	s_waitcnt vmcnt(0)
	v_exp_f32_e32 v175, v162
	v_exp_f32_e32 v177, v163
	v_exp_f32_e32 v173, v164
	v_exp_f32_e32 v176, v165
	v_exp_f32_e32 v172, v166
	v_exp_f32_e32 v174, v167
	v_exp_f32_e32 v170, v168
	v_exp_f32_e32 v171, v169
	v_exp_f32_e32 v165, v181
	v_exp_f32_e32 v168, v182
	v_exp_f32_e32 v163, v124
	v_exp_f32_e32 v166, v125
	v_exp_f32_e32 v162, v126
	v_exp_f32_e32 v169, v127
	v_exp_f32_e32 v164, v128
	v_exp_f32_e32 v167, v183
	v_pk_fma_f32 v[128:129], v[98:99], s[14:15], v[180:181] op_sel_hi:[1,0,0]
	v_add_f32_e32 v98, v230, v231
	v_fmac_f32_e32 v98, v227, v228
	v_add_f32_e32 v228, v234, v235
	s_add_i32 s8, s31, 2
	s_addk_i32 s30, 0x80
	s_add_i32 s0, s31, 1
	v_pk_fma_f32 v[114:115], v[112:113], s[14:15], v[180:181] op_sel_hi:[1,0,0]
	v_pk_fma_f32 v[116:117], v[110:111], s[14:15], v[180:181] op_sel_hi:[1,0,0]
	v_pk_fma_f32 v[118:119], v[108:109], s[14:15], v[180:181] op_sel_hi:[1,0,0]
	v_pk_fma_f32 v[120:121], v[106:107], s[14:15], v[180:181] op_sel_hi:[1,0,0]
	v_pk_fma_f32 v[122:123], v[104:105], s[14:15], v[180:181] op_sel_hi:[1,0,0]
	v_pk_fma_f32 v[124:125], v[102:103], s[14:15], v[180:181] op_sel_hi:[1,0,0]
	v_pk_fma_f32 v[126:127], v[100:101], s[14:15], v[180:181] op_sel_hi:[1,0,0]
	v_fmac_f32_e32 v228, v98, v232
	s_cmp_ge_i32 s0, s51
	v_add_u32_e32 v229, 0xffffff80, v229
	s_waitcnt lgkmcnt(0)
	s_barrier
	s_cbranch_scc1 .LBB0_852
	s_mov_b32 s31, s8
	v_mov_b32_e32 v227, v179
	s_branch .LBB0_833

.LBB0_999:
	v_add_u32_e32 v0, 0x410, v145
	s_waitcnt vmcnt(31)
	ds_write2_b32 v145, v66, v67 offset1:1
	ds_write2_b32 v145, v68, v69 offset0:2 offset1:3
	s_waitcnt vmcnt(30)
	ds_write2_b32 v0, v70, v71 offset1:1
	v_add_u32_e32 v0, 0x418, v145
	ds_write2_b32 v0, v72, v73 offset1:1
	v_add_u32_e32 v0, 0x820, v145
	s_waitcnt vmcnt(29)
	ds_write2_b32 v0, v74, v75 offset1:1
	v_add_u32_e32 v0, 0x828, v145
	ds_write2_b32 v0, v76, v77 offset1:1
	v_add_u32_e32 v0, 0xc30, v145
	s_waitcnt vmcnt(28)
	ds_write2_b32 v0, v78, v79 offset1:1
	v_add_u32_e32 v0, 0xc38, v145
	ds_write2_b32 v0, v80, v81 offset1:1
	v_add_u32_e32 v0, 0x1040, v145
	s_waitcnt vmcnt(27)
	ds_write2_b32 v0, v82, v83 offset1:1
	v_add_u32_e32 v0, 0x1048, v145
	ds_write2_b32 v0, v84, v85 offset1:1
	v_add_u32_e32 v0, 0x1450, v145
	s_waitcnt vmcnt(26)
	ds_write2_b32 v0, v86, v87 offset1:1
	v_add_u32_e32 v0, 0x1458, v145
	ds_write2_b32 v0, v88, v89 offset1:1
	v_add_u32_e32 v0, 0x1860, v145
	s_waitcnt vmcnt(25)
	ds_write2_b32 v0, v90, v91 offset1:1
	v_add_u32_e32 v0, 0x1868, v145
	ds_write2_b32 v0, v92, v93 offset1:1
	v_add_u32_e32 v0, 0x1c70, v145
	s_waitcnt vmcnt(24)
	ds_write2_b32 v0, v94, v95 offset1:1
	v_add_u32_e32 v0, 0x1c78, v145
	ds_write2_b32 v0, v96, v97 offset1:1
	v_add_u32_e32 v0, 0x2080, v145
	s_waitcnt vmcnt(23)
	ds_write2_b32 v0, v98, v99 offset1:1
	v_add_u32_e32 v0, 0x2088, v145
	ds_write2_b32 v0, v100, v101 offset1:1
	v_add_u32_e32 v0, 0x2490, v145
	s_waitcnt vmcnt(22)
	ds_write2_b32 v0, v102, v103 offset1:1
	v_add_u32_e32 v0, 0x2498, v145
	ds_write2_b32 v0, v104, v105 offset1:1
	v_add_u32_e32 v0, 0x28a0, v145
	s_waitcnt vmcnt(21)
	ds_write2_b32 v0, v106, v107 offset1:1
	v_add_u32_e32 v0, 0x28a8, v145
	ds_write2_b32 v0, v108, v109 offset1:1
	v_add_u32_e32 v0, 0x2cb0, v145
	s_waitcnt vmcnt(20)
	ds_write2_b32 v0, v110, v111 offset1:1
	v_add_u32_e32 v0, 0x2cb8, v145
	ds_write2_b32 v0, v112, v113 offset1:1
	v_add_u32_e32 v0, 0x30c0, v145
	s_waitcnt vmcnt(19)
	ds_write2_b32 v0, v114, v115 offset1:1
	v_add_u32_e32 v0, 0x30c8, v145
	ds_write2_b32 v0, v116, v117 offset1:1
	v_add_u32_e32 v0, 0x34d0, v145
	s_waitcnt vmcnt(18)
	ds_write2_b32 v0, v118, v119 offset1:1
	v_add_u32_e32 v0, 0x34d8, v145
	ds_write2_b32 v0, v120, v121 offset1:1
	v_add_u32_e32 v0, 0x38e0, v145
	s_waitcnt vmcnt(17)
	ds_write2_b32 v0, v122, v123 offset1:1
	v_add_u32_e32 v0, 0x38e8, v145
	ds_write2_b32 v0, v124, v125 offset1:1
	v_add_u32_e32 v0, 0x3cf0, v145
	s_waitcnt vmcnt(16)
	ds_write2_b32 v0, v126, v127 offset1:1
	v_add_u32_e32 v0, 0x3cf8, v145
	ds_write2_b32 v0, v128, v129 offset1:1
	s_waitcnt lgkmcnt(0)
	ds_read2_b32 v[70:71], v144 offset1:16
	ds_read2_b32 v[72:73], v144 offset0:65 offset1:81
	ds_read2_b32 v[74:75], v144 offset0:130 offset1:146
	ds_read2_b32 v[76:77], v144 offset0:195 offset1:211
	v_mov_b32_e32 v66, 0
	s_waitcnt lgkmcnt(3)
	v_mul_f32_e32 v0, 0x43800000, v70
	s_waitcnt lgkmcnt(2)
	v_mul_f32_e32 v67, 0x43800000, v72
	v_cvt_pk_fp8_f32 v66, v0, v67
	v_add_u32_e32 v0, 0x400, v144
	ds_read2_b32 v[78:79], v0 offset0:4 offset1:20
	ds_read2_b32 v[80:81], v0 offset0:69 offset1:85
	ds_read2_b32 v[82:83], v0 offset0:134 offset1:150
	s_waitcnt lgkmcnt(4)
	v_mul_f32_e32 v68, 0x43800000, v74
	s_waitcnt lgkmcnt(3)
	v_mul_f32_e32 v67, 0x43800000, v76
	ds_read2_b32 v[84:85], v0 offset0:199 offset1:215
	v_add_u32_e32 v106, 0x800, v144
	v_cvt_pk_fp8_f32 v66, v68, v67 op_sel:[0,0,1]
	s_waitcnt lgkmcnt(3)
	v_mul_f32_e32 v68, 0x43800000, v78
	s_waitcnt lgkmcnt(2)
	v_mul_f32_e32 v69, 0x43800000, v80
	v_mov_b32_e32 v67, 0
	ds_read2_b32 v[86:87], v106 offset0:8 offset1:24
	ds_read2_b32 v[88:89], v106 offset0:73 offset1:89
	v_add_u32_e32 v107, 0xc00, v144
	v_cvt_pk_fp8_f32 v67, v68, v69
	ds_read2_b32 v[90:91], v106 offset0:138 offset1:154
	ds_read2_b32 v[92:93], v106 offset0:203 offset1:219
	ds_read2_b32 v[94:95], v107 offset0:12 offset1:28
	ds_read2_b32 v[96:97], v107 offset0:77 offset1:93
	s_ashr_i32 s0, s29, 11
	s_ashr_i32 s1, s0, 31
	s_lshl_b64 s[0:1], s[0:1], 23
	s_waitcnt lgkmcnt(7)
	v_mul_f32_e32 v70, 0x43800000, v82
	s_waitcnt lgkmcnt(6)
	v_mul_f32_e32 v68, 0x43800000, v84
	s_add_u32 s0, s9, s0
	v_cvt_pk_fp8_f32 v67, v70, v68 op_sel:[0,0,1]
	s_waitcnt lgkmcnt(5)
	v_mul_f32_e32 v69, 0x43800000, v86
	s_waitcnt lgkmcnt(4)
	v_mul_f32_e32 v70, 0x43800000, v88
	v_mov_b32_e32 v68, 0
	ds_read2_b32 v[98:99], v107 offset0:142 offset1:158
	ds_read2_b32 v[100:101], v107 offset0:207 offset1:223
	s_addc_u32 s1, s10, s1
	s_and_b32 s2, s25, 0x3f0
	s_bfe_u32 s3, s29, 0x40007
	v_cvt_pk_fp8_f32 v68, v69, v70
	s_waitcnt lgkmcnt(3)
	v_mul_f32_e32 v70, 0x43800000, v94
	s_waitcnt lgkmcnt(2)
	v_mul_f32_e32 v76, 0x43800000, v96
	v_mov_b32_e32 v69, 0
	s_or_b32 s2, s2, s3
	v_cvt_pk_fp8_f32 v69, v70, v76
	s_lshl_b32 s2, s2, 13
	s_add_u32 s0, s0, s2
	v_mul_f32_e32 v72, 0x43800000, v90
	v_mul_f32_e32 v74, 0x43800000, v92
	s_addc_u32 s1, s1, 0
	s_and_b32 s2, s29, 64
	v_cvt_pk_fp8_f32 v68, v72, v74 op_sel:[0,0,1]
	s_waitcnt lgkmcnt(1)
	v_mul_f32_e32 v70, 0x43800000, v98
	s_waitcnt lgkmcnt(0)
	v_mul_f32_e32 v72, 0x43800000, v100
	s_add_u32 s0, s0, s2
	v_cvt_pk_fp8_f32 v69, v70, v72 op_sel:[0,0,1]
	s_addc_u32 s1, s1, 0
	v_lshl_add_u64 v[102:103], s[0:1], 0, v[132:133]
	v_lshl_add_u64 v[104:105], v[102:103], 0, v[134:135]
	global_store_dwordx4 v[104:105], v[66:69], off nt
	v_mul_f32_e32 v70, 0x43800000, v77
	v_mul_f32_e32 v72, 0x43800000, v93
	v_mul_f32_e32 v67, 0x43800000, v71
	v_mul_f32_e32 v68, 0x43800000, v73
	v_mov_b32_e32 v66, 0
	v_cvt_pk_fp8_f32 v66, v67, v68
	v_mul_f32_e32 v68, 0x43800000, v79
	v_mul_f32_e32 v71, 0x43800000, v81
	v_mov_b32_e32 v67, 0
	v_cvt_pk_fp8_f32 v67, v68, v71
	v_mul_f32_e32 v69, 0x43800000, v75
	v_cvt_pk_fp8_f32 v66, v69, v70 op_sel:[0,0,1]
	v_mul_f32_e32 v68, 0x43800000, v83
	v_mul_f32_e32 v69, 0x43800000, v85
	v_cvt_pk_fp8_f32 v67, v68, v69 op_sel:[0,0,1]
	v_mul_f32_e32 v69, 0x43800000, v87
	v_mul_f32_e32 v70, 0x43800000, v89
	v_mov_b32_e32 v68, 0
	v_cvt_pk_fp8_f32 v68, v69, v70
	v_mul_f32_e32 v70, 0x43800000, v95
	v_mul_f32_e32 v73, 0x43800000, v97
	v_mov_b32_e32 v69, 0
	v_cvt_pk_fp8_f32 v69, v70, v73
	v_mul_f32_e32 v71, 0x43800000, v91
	v_cvt_pk_fp8_f32 v68, v71, v72 op_sel:[0,0,1]
	v_mul_f32_e32 v70, 0x43800000, v99
	v_mul_f32_e32 v71, 0x43800000, v101
	v_cvt_pk_fp8_f32 v69, v70, v71 op_sel:[0,0,1]
	ds_read2_b32 v[70:71], v144 offset0:32 offset1:48
	ds_read2_b32 v[72:73], v144 offset0:97 offset1:113
	ds_read2_b32 v[74:75], v144 offset0:162 offset1:178
	v_lshl_add_u64 v[76:77], v[102:103], 0, v[136:137]
	s_add_i32 s24, s24, s8
	global_store_dwordx4 v[76:77], v[66:69], off nt
	ds_read2_b32 v[76:77], v144 offset0:227 offset1:243
	ds_read2_b32 v[78:79], v0 offset0:36 offset1:52
	ds_read2_b32 v[80:81], v0 offset0:101 offset1:117
	s_waitcnt lgkmcnt(5)
	v_mul_f32_e32 v67, 0x43800000, v70
	s_waitcnt lgkmcnt(4)
	v_mul_f32_e32 v68, 0x43800000, v72
	v_mov_b32_e32 v66, 0
	v_cvt_pk_fp8_f32 v66, v67, v68
	s_waitcnt lgkmcnt(3)
	v_mul_f32_e32 v69, 0x43800000, v74
	s_waitcnt lgkmcnt(2)
	v_mul_f32_e32 v67, 0x43800000, v76
	ds_read2_b32 v[82:83], v0 offset0:166 offset1:182
	ds_read2_b32 v[84:85], v0 offset0:231 offset1:247
	v_cvt_pk_fp8_f32 v66, v69, v67 op_sel:[0,0,1]
	s_waitcnt lgkmcnt(3)
	v_mul_f32_e32 v68, 0x43800000, v78
	s_waitcnt lgkmcnt(2)
	v_mul_f32_e32 v69, 0x43800000, v80
	v_mov_b32_e32 v67, 0
	ds_read2_b32 v[86:87], v106 offset0:40 offset1:56
	v_cvt_pk_fp8_f32 v67, v68, v69
	ds_read2_b32 v[88:89], v106 offset0:105 offset1:121
	ds_read2_b32 v[90:91], v106 offset0:170 offset1:186
	ds_read2_b32 v[92:93], v106 offset0:235 offset1:251
	ds_read2_b32 v[94:95], v107 offset0:44 offset1:60
	ds_read2_b32 v[96:97], v107 offset0:109 offset1:125
	s_waitcnt lgkmcnt(7)
	v_mul_f32_e32 v0, 0x43800000, v82
	s_waitcnt lgkmcnt(6)
	v_mul_f32_e32 v68, 0x43800000, v84
	v_cvt_pk_fp8_f32 v67, v0, v68 op_sel:[0,0,1]
	s_waitcnt lgkmcnt(5)
	v_mul_f32_e32 v0, 0x43800000, v86
	s_waitcnt lgkmcnt(4)
	v_mul_f32_e32 v69, 0x43800000, v88
	v_mov_b32_e32 v68, 0
	ds_read2_b32 v[98:99], v107 offset0:174 offset1:190
	ds_read2_b32 v[100:101], v107 offset0:239 offset1:255
	v_cvt_pk_fp8_f32 v68, v0, v69
	s_waitcnt lgkmcnt(3)
	v_mul_f32_e32 v0, 0x43800000, v94
	s_waitcnt lgkmcnt(2)
	v_mul_f32_e32 v74, 0x43800000, v96
	v_mov_b32_e32 v69, 0
	v_cvt_pk_fp8_f32 v69, v0, v74
	v_mul_f32_e32 v70, 0x43800000, v90
	v_mul_f32_e32 v72, 0x43800000, v92
	v_cvt_pk_fp8_f32 v68, v70, v72 op_sel:[0,0,1]
	s_waitcnt lgkmcnt(1)
	v_mul_f32_e32 v0, 0x43800000, v98
	s_waitcnt lgkmcnt(0)
	v_mul_f32_e32 v70, 0x43800000, v100
	v_cvt_pk_fp8_f32 v69, v0, v70 op_sel:[0,0,1]
	v_mul_f32_e32 v0, 0x43800000, v71
	v_mul_f32_e32 v71, 0x43800000, v73
	v_mov_b32_e32 v70, 0
	v_cvt_pk_fp8_f32 v70, v0, v71
	v_mul_f32_e32 v0, 0x43800000, v79
	v_mul_f32_e32 v74, 0x43800000, v81
	v_mov_b32_e32 v71, 0
	v_cvt_pk_fp8_f32 v71, v0, v74
	v_mul_f32_e32 v72, 0x43800000, v75
	v_mul_f32_e32 v73, 0x43800000, v77
	v_cvt_pk_fp8_f32 v70, v72, v73 op_sel:[0,0,1]
	v_mul_f32_e32 v0, 0x43800000, v83
	v_mul_f32_e32 v72, 0x43800000, v85
	v_cvt_pk_fp8_f32 v71, v0, v72 op_sel:[0,0,1]
	v_mul_f32_e32 v0, 0x43800000, v87
	v_mul_f32_e32 v73, 0x43800000, v89
	v_mov_b32_e32 v72, 0
	v_cvt_pk_fp8_f32 v72, v0, v73
	v_mul_f32_e32 v0, 0x43800000, v95
	v_mul_f32_e32 v76, 0x43800000, v97
	v_mov_b32_e32 v73, 0
	v_cvt_pk_fp8_f32 v73, v0, v76
	v_mul_f32_e32 v74, 0x43800000, v91
	v_mul_f32_e32 v75, 0x43800000, v93
	v_cvt_pk_fp8_f32 v72, v74, v75 op_sel:[0,0,1]
	v_mul_f32_e32 v0, 0x43800000, v99
	v_mul_f32_e32 v74, 0x43800000, v101
	v_cvt_pk_fp8_f32 v73, v0, v74 op_sel:[0,0,1]
	v_lshl_add_u64 v[74:75], v[102:103], 0, v[138:139]
	global_store_dwordx4 v[74:75], v[66:69], off nt
	s_add_i32 s0, s23, s24
	s_add_i32 s25, s25, s26
	v_lshl_add_u64 v[66:67], v[102:103], 0, v[140:141]
	global_store_dwordx4 v[66:67], v[70:73], off nt
	s_waitcnt lgkmcnt(0)
	s_add_i32 s28, s28, s15
	s_waitcnt vmcnt(4)
	v_mov_b64_e32 v[68:69], v[4:5]
	v_mov_b64_e32 v[72:73], v[8:9]
	v_mov_b64_e32 v[76:77], v[12:13]
	v_mov_b64_e32 v[80:81], v[16:17]
	v_mov_b64_e32 v[84:85], v[20:21]
	v_mov_b64_e32 v[88:89], v[24:25]
	v_mov_b64_e32 v[92:93], v[28:29]
	v_mov_b64_e32 v[96:97], v[32:33]
	v_mov_b64_e32 v[100:101], v[36:37]
	v_mov_b64_e32 v[104:105], v[40:41]
	v_mov_b64_e32 v[108:109], v[44:45]
	v_mov_b64_e32 v[112:113], v[48:49]
	v_mov_b64_e32 v[116:117], v[52:53]
	v_mov_b64_e32 v[120:121], v[56:57]
	v_mov_b64_e32 v[124:125], v[60:61]
	v_mov_b64_e32 v[128:129], v[64:65]
	s_cmp_lt_i32 s0, 0xbf68
	v_mov_b64_e32 v[66:67], v[2:3]
	v_mov_b64_e32 v[70:71], v[6:7]
	v_mov_b64_e32 v[74:75], v[10:11]
	v_mov_b64_e32 v[78:79], v[14:15]
	v_mov_b64_e32 v[82:83], v[18:19]
	v_mov_b64_e32 v[86:87], v[22:23]
	v_mov_b64_e32 v[90:91], v[26:27]
	v_mov_b64_e32 v[94:95], v[30:31]
	v_mov_b64_e32 v[98:99], v[34:35]
	v_mov_b64_e32 v[102:103], v[38:39]
	v_mov_b64_e32 v[106:107], v[42:43]
	v_mov_b64_e32 v[110:111], v[46:47]
	v_mov_b64_e32 v[114:115], v[50:51]
	v_mov_b64_e32 v[118:119], v[54:55]
	v_mov_b64_e32 v[122:123], v[58:59]
	v_mov_b64_e32 v[126:127], v[62:63]
	s_cbranch_scc0 .LBB0_1002

.Lcv4_last:
	s_waitcnt vmcnt(0)
	s_branch .LBB0_999

.LBB0_1057:
	s_cmp_gt_i32 s72, 5
	s_cselect_b64 s[0:1], -1, 0
	s_cmp_lt_i32 s73, 6
	s_cselect_b64 s[2:3], -1, 0
	s_or_b64 s[0:1], s[0:1], s[2:3]
	s_and_b64 vcc, exec, s[0:1]
	s_cbranch_vccnz .LBB0_1111
	s_waitcnt vmcnt(0)
	v_mov_b32_e32 v2, v254
	s_mov_b32 s0, 0x400000
	v_lshl_add_u32 v1, s82, 9, v2
	v_cmp_gt_i32_e32 vcc, s0, v1
	s_and_saveexec_b64 s[4:5], vcc
	s_cbranch_execz .LBB0_1061
	s_add_u32 s6, s86, 0x45800000
	s_addc_u32 s7, s87, 0
	s_add_u32 s8, s86, 0x31800000
	s_addc_u32 s9, s87, 0
	s_add_u32 s10, s86, 0x7000000
	s_addc_u32 s11, s87, 0
	s_add_u32 s12, s86, 0xb000000
	v_lshlrev_b32_e32 v0, 3, v2
	s_addc_u32 s13, s87, 0
	s_lshl_b32 s18, s88, 9
	v_lshl_add_u32 v4, s82, 12, v0
	s_lshl_b32 s19, s88, 12
	s_mov_b64 s[14:15], 0
	v_mov_b32_e32 v3, 0
	v_mov_b32_e32 v43, 0
	v_mov_b32_e32 v83, 0
	v_mov_b32_e32 v123, 0
	s_mov_b64 s[16:17], 0xf008840
	s_mov_b32 s20, 0xf008000
	s_mov_b32 s21, 0xffff0000
	s_movk_i32 s22, 0x7fff
	s_mov_b32 s23, 0x3fffff
.LBB0_1060:
	v_ashrrev_i32_e32 v6, 8, v1
	v_bfe_u32 v2, v4, 7, 4
	v_mul_hi_i32_i24_e32 v9, 0x8a00, v6
	v_mul_i32_i24_e32 v8, 0x8a00, v6
	v_mul_u32_u24_e32 v2, 3, v2
	v_ashrrev_i32_e32 v7, 31, v6
	v_lshl_add_u64 v[8:9], s[86:87], 0, v[8:9]
	v_lshlrev_b32_e32 v2, 1, v2
	v_lshlrev_b64 v[18:19], 12, v[6:7]
	v_lshl_add_u64 v[6:7], v[8:9], 0, v[2:3]
	v_and_b32_e32 v0, 0x7f8, v4
	v_add_co_u32_e32 v22, vcc, s20, v6
	v_lshl_or_b32 v18, v0, 1, v18
	s_nop 0
	v_addc_co_u32_e32 v23, vcc, 0, v7, vcc
	v_lshl_add_u64 v[20:21], v[6:7], 0, s[16:17]
	v_lshl_add_u64 v[24:25], s[6:7], 0, v[18:19]
	v_lshl_add_u64 v[26:27], s[8:9], 0, v[18:19]
	v_lshl_add_u64 v[28:29], s[10:11], 0, v[18:19]
	global_load_dword v0, v[22:23], off offset:2112
	global_load_dwordx4 v[6:9], v[24:25], off
	global_load_ushort v2, v[20:21], off offset:4
	global_load_dwordx4 v[10:13], v[26:27], off
	global_load_dwordx4 v[14:17], v[28:29], off
	v_add_u32_e32 v1, s18, v1
	v_add_u32_e32 v4, s19, v4
	v_ashrrev_i32_e32 v46, 8, v1
	v_bfe_u32 v42, v4, 7, 4
	v_mul_hi_i32_i24_e32 v49, 0x8a00, v46
	v_mul_i32_i24_e32 v48, 0x8a00, v46
	v_mul_u32_u24_e32 v42, 3, v42
	v_ashrrev_i32_e32 v47, 31, v46
	v_lshl_add_u64 v[48:49], s[86:87], 0, v[48:49]
	v_lshlrev_b32_e32 v42, 1, v42
	v_lshlrev_b64 v[58:59], 12, v[46:47]
	v_lshl_add_u64 v[46:47], v[48:49], 0, v[42:43]
	v_and_b32_e32 v40, 0x7f8, v4
	v_add_co_u32_e32 v62, vcc, s20, v46
	v_lshl_or_b32 v58, v40, 1, v58
	s_nop 0
	v_addc_co_u32_e32 v63, vcc, 0, v47, vcc
	v_lshl_add_u64 v[60:61], v[46:47], 0, s[16:17]
	v_lshl_add_u64 v[64:65], s[6:7], 0, v[58:59]
	v_lshl_add_u64 v[66:67], s[8:9], 0, v[58:59]
	v_lshl_add_u64 v[68:69], s[10:11], 0, v[58:59]
	global_load_dword v40, v[62:63], off offset:2112
	global_load_dwordx4 v[46:49], v[64:65], off
	global_load_ushort v42, v[60:61], off offset:4
	global_load_dwordx4 v[50:53], v[66:67], off
	global_load_dwordx4 v[54:57], v[68:69], off
	v_add_u32_e32 v1, s18, v1
	v_add_u32_e32 v4, s19, v4
	v_ashrrev_i32_e32 v86, 8, v1
	v_bfe_u32 v82, v4, 7, 4
	v_mul_hi_i32_i24_e32 v89, 0x8a00, v86
	v_mul_i32_i24_e32 v88, 0x8a00, v86
	v_mul_u32_u24_e32 v82, 3, v82
	v_ashrrev_i32_e32 v87, 31, v86
	v_lshl_add_u64 v[88:89], s[86:87], 0, v[88:89]
	v_lshlrev_b32_e32 v82, 1, v82
	v_lshlrev_b64 v[98:99], 12, v[86:87]
	v_lshl_add_u64 v[86:87], v[88:89], 0, v[82:83]
	v_and_b32_e32 v80, 0x7f8, v4
	v_add_co_u32_e32 v102, vcc, s20, v86
	v_lshl_or_b32 v98, v80, 1, v98
	s_nop 0
	v_addc_co_u32_e32 v103, vcc, 0, v87, vcc
	v_lshl_add_u64 v[100:101], v[86:87], 0, s[16:17]
	v_lshl_add_u64 v[104:105], s[6:7], 0, v[98:99]
	v_lshl_add_u64 v[106:107], s[8:9], 0, v[98:99]
	v_lshl_add_u64 v[108:109], s[10:11], 0, v[98:99]
	global_load_dword v80, v[102:103], off offset:2112
	global_load_dwordx4 v[86:89], v[104:105], off
	global_load_ushort v82, v[100:101], off offset:4
	global_load_dwordx4 v[90:93], v[106:107], off
	global_load_dwordx4 v[94:97], v[108:109], off
	v_add_u32_e32 v1, s18, v1
	v_add_u32_e32 v4, s19, v4
	v_ashrrev_i32_e32 v126, 8, v1
	v_bfe_u32 v122, v4, 7, 4
	v_mul_hi_i32_i24_e32 v129, 0x8a00, v126
	v_mul_i32_i24_e32 v128, 0x8a00, v126
	v_mul_u32_u24_e32 v122, 3, v122
	v_ashrrev_i32_e32 v127, 31, v126
	v_lshl_add_u64 v[128:129], s[86:87], 0, v[128:129]
	v_lshlrev_b32_e32 v122, 1, v122
	v_lshlrev_b64 v[138:139], 12, v[126:127]
	v_lshl_add_u64 v[126:127], v[128:129], 0, v[122:123]
	v_and_b32_e32 v120, 0x7f8, v4
	v_add_co_u32_e32 v142, vcc, s20, v126
	v_lshl_or_b32 v138, v120, 1, v138
	s_nop 0
	v_addc_co_u32_e32 v143, vcc, 0, v127, vcc
	v_lshl_add_u64 v[140:141], v[126:127], 0, s[16:17]
	v_lshl_add_u64 v[144:145], s[6:7], 0, v[138:139]
	v_lshl_add_u64 v[146:147], s[8:9], 0, v[138:139]
	v_lshl_add_u64 v[148:149], s[10:11], 0, v[138:139]
	global_load_dword v120, v[142:143], off offset:2112
	global_load_dwordx4 v[126:129], v[144:145], off
	global_load_ushort v122, v[140:141], off offset:4
	global_load_dwordx4 v[130:133], v[146:147], off
	global_load_dwordx4 v[134:137], v[148:149], off
	v_add_u32_e32 v1, s18, v1
	v_cmp_lt_i32_e32 vcc, s23, v1
	v_add_u32_e32 v4, s19, v4
	s_or_b64 s[14:15], vcc, s[14:15]
	v_lshl_add_u64 v[18:19], s[12:13], 0, v[18:19]
	v_lshl_add_u64 v[58:59], s[12:13], 0, v[58:59]
	v_lshl_add_u64 v[98:99], s[12:13], 0, v[98:99]
	v_lshl_add_u64 v[138:139], s[12:13], 0, v[138:139]
	s_waitcnt vmcnt(19)
	v_lshlrev_b32_e32 v5, 16, v0
	v_and_b32_e32 v0, 0xffff0000, v0
	v_mul_f32_e32 v0, 0xbfb8aa3b, v0
	s_waitcnt vmcnt(17)
	v_lshlrev_b32_e32 v2, 16, v2
	v_mul_f32_e32 v5, 0xbfb8aa3b, v5
	v_exp_f32_e32 v0, v0
	v_mul_f32_e32 v2, 0xbfb8aa3b, v2
	v_exp_f32_e32 v5, v5
	v_exp_f32_e32 v2, v2
	v_add_f32_e32 v0, 1.0, v0
	v_rcp_f32_e32 v0, v0
	v_add_f32_e32 v5, 1.0, v5
	v_add_f32_e32 v32, 1.0, v2
	v_rcp_f32_e32 v2, v5
	v_rcp_f32_e32 v32, v32
	s_waitcnt vmcnt(16)
	v_lshlrev_b32_e32 v23, 16, v11
	v_lshlrev_b32_e32 v22, 16, v10
	v_and_b32_e32 v11, 0xffff0000, v11
	v_and_b32_e32 v10, 0xffff0000, v10
	v_lshlrev_b32_e32 v29, 16, v13
	v_lshlrev_b32_e32 v28, 16, v12
	v_and_b32_e32 v13, 0xffff0000, v13
	v_and_b32_e32 v12, 0xffff0000, v12
	v_lshlrev_b32_e32 v21, 16, v7
	v_lshlrev_b32_e32 v20, 16, v6
	v_and_b32_e32 v7, 0xffff0000, v7
	v_and_b32_e32 v6, 0xffff0000, v6
	v_lshlrev_b32_e32 v27, 16, v9
	v_lshlrev_b32_e32 v26, 16, v8
	v_and_b32_e32 v9, 0xffff0000, v9
	v_and_b32_e32 v8, 0xffff0000, v8
	v_pk_mul_f32 v[22:23], v[0:1], v[22:23] op_sel_hi:[0,1]
	v_pk_mul_f32 v[10:11], v[0:1], v[10:11] op_sel_hi:[0,1]
	v_pk_mul_f32 v[28:29], v[0:1], v[28:29] op_sel_hi:[0,1]
	v_pk_mul_f32 v[12:13], v[0:1], v[12:13] op_sel_hi:[0,1]
	s_waitcnt vmcnt(15)
	v_lshlrev_b32_e32 v25, 16, v15
	v_lshlrev_b32_e32 v24, 16, v14
	v_and_b32_e32 v15, 0xffff0000, v15
	v_and_b32_e32 v14, 0xffff0000, v14
	v_lshlrev_b32_e32 v31, 16, v17
	v_lshlrev_b32_e32 v30, 16, v16
	v_and_b32_e32 v17, 0xffff0000, v17
	v_and_b32_e32 v16, 0xffff0000, v16
	v_pk_fma_f32 v[20:21], v[2:3], v[20:21], v[22:23] op_sel_hi:[0,1,1]
	v_pk_fma_f32 v[6:7], v[2:3], v[6:7], v[10:11] op_sel_hi:[0,1,1]
	v_pk_fma_f32 v[10:11], v[2:3], v[26:27], v[28:29] op_sel_hi:[0,1,1]
	v_pk_fma_f32 v[8:9], v[2:3], v[8:9], v[12:13] op_sel_hi:[0,1,1]
	v_pk_fma_f32 v[12:13], v[32:33], v[24:25], v[20:21] op_sel_hi:[0,1,1]
	v_pk_fma_f32 v[6:7], v[32:33], v[14:15], v[6:7] op_sel_hi:[0,1,1]
	v_pk_fma_f32 v[10:11], v[32:33], v[30:31], v[10:11] op_sel_hi:[0,1,1]
	v_pk_fma_f32 v[8:9], v[32:33], v[16:17], v[8:9] op_sel_hi:[0,1,1]
	v_bfe_u32 v0, v9, 16, 1
	v_bfe_u32 v2, v8, 16, 1
	v_bfe_u32 v5, v7, 16, 1
	v_bfe_u32 v15, v12, 16, 1
	v_bfe_u32 v16, v13, 16, 1
	v_bfe_u32 v17, v10, 16, 1
	v_bfe_u32 v20, v11, 16, 1
	v_bfe_u32 v14, v6, 16, 1
	v_add3_u32 v5, v7, v5, s22
	v_add3_u32 v2, v8, v2, s22
	v_add3_u32 v0, v9, v0, s22
	v_add3_u32 v7, v11, v20, s22
	v_add3_u32 v8, v10, v17, s22
	v_add3_u32 v9, v13, v16, s22
	v_add3_u32 v10, v12, v15, s22
	v_add3_u32 v6, v6, v14, s22
	v_lshrrev_b32_e32 v10, 16, v10
	v_lshrrev_b32_e32 v11, 16, v9
	v_lshrrev_b32_e32 v8, 16, v8
	v_lshrrev_b32_e32 v7, 16, v7
	v_and_or_b32 v9, v0, s21, v7
	v_and_or_b32 v8, v2, s21, v8
	v_and_or_b32 v7, v5, s21, v11
	v_and_or_b32 v6, v6, s21, v10
	global_store_dwordx4 v[18:19], v[6:9], off
	s_waitcnt vmcnt(15)
	v_lshlrev_b32_e32 v45, 16, v40
	v_and_b32_e32 v40, 0xffff0000, v40
	v_mul_f32_e32 v40, 0xbfb8aa3b, v40
	s_waitcnt vmcnt(13)
	v_lshlrev_b32_e32 v42, 16, v42
	v_mul_f32_e32 v45, 0xbfb8aa3b, v45
	v_exp_f32_e32 v40, v40
	v_mul_f32_e32 v42, 0xbfb8aa3b, v42
	v_exp_f32_e32 v45, v45
	v_exp_f32_e32 v42, v42
	v_add_f32_e32 v40, 1.0, v40
	v_rcp_f32_e32 v40, v40
	v_add_f32_e32 v45, 1.0, v45
	v_add_f32_e32 v72, 1.0, v42
	v_rcp_f32_e32 v42, v45
	v_rcp_f32_e32 v72, v72
	s_waitcnt vmcnt(12)
	v_lshlrev_b32_e32 v63, 16, v51
	v_lshlrev_b32_e32 v62, 16, v50
	v_and_b32_e32 v51, 0xffff0000, v51
	v_and_b32_e32 v50, 0xffff0000, v50
	v_lshlrev_b32_e32 v69, 16, v53
	v_lshlrev_b32_e32 v68, 16, v52
	v_and_b32_e32 v53, 0xffff0000, v53
	v_and_b32_e32 v52, 0xffff0000, v52
	v_lshlrev_b32_e32 v61, 16, v47
	v_lshlrev_b32_e32 v60, 16, v46
	v_and_b32_e32 v47, 0xffff0000, v47
	v_and_b32_e32 v46, 0xffff0000, v46
	v_lshlrev_b32_e32 v67, 16, v49
	v_lshlrev_b32_e32 v66, 16, v48
	v_and_b32_e32 v49, 0xffff0000, v49
	v_and_b32_e32 v48, 0xffff0000, v48
	v_pk_mul_f32 v[62:63], v[40:41], v[62:63] op_sel_hi:[0,1]
	v_pk_mul_f32 v[50:51], v[40:41], v[50:51] op_sel_hi:[0,1]
	v_pk_mul_f32 v[68:69], v[40:41], v[68:69] op_sel_hi:[0,1]
	v_pk_mul_f32 v[52:53], v[40:41], v[52:53] op_sel_hi:[0,1]
	s_waitcnt vmcnt(11)
	v_lshlrev_b32_e32 v65, 16, v55
	v_lshlrev_b32_e32 v64, 16, v54
	v_and_b32_e32 v55, 0xffff0000, v55
	v_and_b32_e32 v54, 0xffff0000, v54
	v_lshlrev_b32_e32 v71, 16, v57
	v_lshlrev_b32_e32 v70, 16, v56
	v_and_b32_e32 v57, 0xffff0000, v57
	v_and_b32_e32 v56, 0xffff0000, v56
	v_pk_fma_f32 v[60:61], v[42:43], v[60:61], v[62:63] op_sel_hi:[0,1,1]
	v_pk_fma_f32 v[46:47], v[42:43], v[46:47], v[50:51] op_sel_hi:[0,1,1]
	v_pk_fma_f32 v[50:51], v[42:43], v[66:67], v[68:69] op_sel_hi:[0,1,1]
	v_pk_fma_f32 v[48:49], v[42:43], v[48:49], v[52:53] op_sel_hi:[0,1,1]
	v_pk_fma_f32 v[52:53], v[72:73], v[64:65], v[60:61] op_sel_hi:[0,1,1]
	v_pk_fma_f32 v[46:47], v[72:73], v[54:55], v[46:47] op_sel_hi:[0,1,1]
	v_pk_fma_f32 v[50:51], v[72:73], v[70:71], v[50:51] op_sel_hi:[0,1,1]
	v_pk_fma_f32 v[48:49], v[72:73], v[56:57], v[48:49] op_sel_hi:[0,1,1]
	v_bfe_u32 v40, v49, 16, 1
	v_bfe_u32 v42, v48, 16, 1
	v_bfe_u32 v45, v47, 16, 1
	v_bfe_u32 v55, v52, 16, 1
	v_bfe_u32 v56, v53, 16, 1
	v_bfe_u32 v57, v50, 16, 1
	v_bfe_u32 v60, v51, 16, 1
	v_bfe_u32 v54, v46, 16, 1
	v_add3_u32 v45, v47, v45, s22
	v_add3_u32 v42, v48, v42, s22
	v_add3_u32 v40, v49, v40, s22
	v_add3_u32 v47, v51, v60, s22
	v_add3_u32 v48, v50, v57, s22
	v_add3_u32 v49, v53, v56, s22
	v_add3_u32 v50, v52, v55, s22
	v_add3_u32 v46, v46, v54, s22
	v_lshrrev_b32_e32 v50, 16, v50
	v_lshrrev_b32_e32 v51, 16, v49
	v_lshrrev_b32_e32 v48, 16, v48
	v_lshrrev_b32_e32 v47, 16, v47
	v_and_or_b32 v49, v40, s21, v47
	v_and_or_b32 v48, v42, s21, v48
	v_and_or_b32 v47, v45, s21, v51
	v_and_or_b32 v46, v46, s21, v50
	global_store_dwordx4 v[58:59], v[46:49], off
	s_waitcnt vmcnt(11)
	v_lshlrev_b32_e32 v85, 16, v80
	v_and_b32_e32 v80, 0xffff0000, v80
	v_mul_f32_e32 v80, 0xbfb8aa3b, v80
	s_waitcnt vmcnt(9)
	v_lshlrev_b32_e32 v82, 16, v82
	v_mul_f32_e32 v85, 0xbfb8aa3b, v85
	v_exp_f32_e32 v80, v80
	v_mul_f32_e32 v82, 0xbfb8aa3b, v82
	v_exp_f32_e32 v85, v85
	v_exp_f32_e32 v82, v82
	v_add_f32_e32 v80, 1.0, v80
	v_rcp_f32_e32 v80, v80
	v_add_f32_e32 v85, 1.0, v85
	v_add_f32_e32 v112, 1.0, v82
	v_rcp_f32_e32 v82, v85
	v_rcp_f32_e32 v112, v112
	s_waitcnt vmcnt(8)
	v_lshlrev_b32_e32 v103, 16, v91
	v_lshlrev_b32_e32 v102, 16, v90
	v_and_b32_e32 v91, 0xffff0000, v91
	v_and_b32_e32 v90, 0xffff0000, v90
	v_lshlrev_b32_e32 v109, 16, v93
	v_lshlrev_b32_e32 v108, 16, v92
	v_and_b32_e32 v93, 0xffff0000, v93
	v_and_b32_e32 v92, 0xffff0000, v92
	v_lshlrev_b32_e32 v101, 16, v87
	v_lshlrev_b32_e32 v100, 16, v86
	v_and_b32_e32 v87, 0xffff0000, v87
	v_and_b32_e32 v86, 0xffff0000, v86
	v_lshlrev_b32_e32 v107, 16, v89
	v_lshlrev_b32_e32 v106, 16, v88
	v_and_b32_e32 v89, 0xffff0000, v89
	v_and_b32_e32 v88, 0xffff0000, v88
	v_pk_mul_f32 v[102:103], v[80:81], v[102:103] op_sel_hi:[0,1]
	v_pk_mul_f32 v[90:91], v[80:81], v[90:91] op_sel_hi:[0,1]
	v_pk_mul_f32 v[108:109], v[80:81], v[108:109] op_sel_hi:[0,1]
	v_pk_mul_f32 v[92:93], v[80:81], v[92:93] op_sel_hi:[0,1]
	s_waitcnt vmcnt(7)
	v_lshlrev_b32_e32 v105, 16, v95
	v_lshlrev_b32_e32 v104, 16, v94
	v_and_b32_e32 v95, 0xffff0000, v95
	v_and_b32_e32 v94, 0xffff0000, v94
	v_lshlrev_b32_e32 v111, 16, v97
	v_lshlrev_b32_e32 v110, 16, v96
	v_and_b32_e32 v97, 0xffff0000, v97
	v_and_b32_e32 v96, 0xffff0000, v96
	v_pk_fma_f32 v[100:101], v[82:83], v[100:101], v[102:103] op_sel_hi:[0,1,1]
	v_pk_fma_f32 v[86:87], v[82:83], v[86:87], v[90:91] op_sel_hi:[0,1,1]
	v_pk_fma_f32 v[90:91], v[82:83], v[106:107], v[108:109] op_sel_hi:[0,1,1]
	v_pk_fma_f32 v[88:89], v[82:83], v[88:89], v[92:93] op_sel_hi:[0,1,1]
	v_pk_fma_f32 v[92:93], v[112:113], v[104:105], v[100:101] op_sel_hi:[0,1,1]
	v_pk_fma_f32 v[86:87], v[112:113], v[94:95], v[86:87] op_sel_hi:[0,1,1]
	v_pk_fma_f32 v[90:91], v[112:113], v[110:111], v[90:91] op_sel_hi:[0,1,1]
	v_pk_fma_f32 v[88:89], v[112:113], v[96:97], v[88:89] op_sel_hi:[0,1,1]
	v_bfe_u32 v80, v89, 16, 1
	v_bfe_u32 v82, v88, 16, 1
	v_bfe_u32 v85, v87, 16, 1
	v_bfe_u32 v95, v92, 16, 1
	v_bfe_u32 v96, v93, 16, 1
	v_bfe_u32 v97, v90, 16, 1
	v_bfe_u32 v100, v91, 16, 1
	v_bfe_u32 v94, v86, 16, 1
	v_add3_u32 v85, v87, v85, s22
	v_add3_u32 v82, v88, v82, s22
	v_add3_u32 v80, v89, v80, s22
	v_add3_u32 v87, v91, v100, s22
	v_add3_u32 v88, v90, v97, s22
	v_add3_u32 v89, v93, v96, s22
	v_add3_u32 v90, v92, v95, s22
	v_add3_u32 v86, v86, v94, s22
	v_lshrrev_b32_e32 v90, 16, v90
	v_lshrrev_b32_e32 v91, 16, v89
	v_lshrrev_b32_e32 v88, 16, v88
	v_lshrrev_b32_e32 v87, 16, v87
	v_and_or_b32 v89, v80, s21, v87
	v_and_or_b32 v88, v82, s21, v88
	v_and_or_b32 v87, v85, s21, v91
	v_and_or_b32 v86, v86, s21, v90
	global_store_dwordx4 v[98:99], v[86:89], off
	s_waitcnt vmcnt(7)
	v_lshlrev_b32_e32 v125, 16, v120
	v_and_b32_e32 v120, 0xffff0000, v120
	v_mul_f32_e32 v120, 0xbfb8aa3b, v120
	s_waitcnt vmcnt(5)
	v_lshlrev_b32_e32 v122, 16, v122
	v_mul_f32_e32 v125, 0xbfb8aa3b, v125
	v_exp_f32_e32 v120, v120
	v_mul_f32_e32 v122, 0xbfb8aa3b, v122
	v_exp_f32_e32 v125, v125
	v_exp_f32_e32 v122, v122
	v_add_f32_e32 v120, 1.0, v120
	v_rcp_f32_e32 v120, v120
	v_add_f32_e32 v125, 1.0, v125
	v_add_f32_e32 v152, 1.0, v122
	v_rcp_f32_e32 v122, v125
	v_rcp_f32_e32 v152, v152
	s_waitcnt vmcnt(4)
	v_lshlrev_b32_e32 v143, 16, v131
	v_lshlrev_b32_e32 v142, 16, v130
	v_and_b32_e32 v131, 0xffff0000, v131
	v_and_b32_e32 v130, 0xffff0000, v130
	v_lshlrev_b32_e32 v149, 16, v133
	v_lshlrev_b32_e32 v148, 16, v132
	v_and_b32_e32 v133, 0xffff0000, v133
	v_and_b32_e32 v132, 0xffff0000, v132
	v_lshlrev_b32_e32 v141, 16, v127
	v_lshlrev_b32_e32 v140, 16, v126
	v_and_b32_e32 v127, 0xffff0000, v127
	v_and_b32_e32 v126, 0xffff0000, v126
	v_lshlrev_b32_e32 v147, 16, v129
	v_lshlrev_b32_e32 v146, 16, v128
	v_and_b32_e32 v129, 0xffff0000, v129
	v_and_b32_e32 v128, 0xffff0000, v128
	v_pk_mul_f32 v[142:143], v[120:121], v[142:143] op_sel_hi:[0,1]
	v_pk_mul_f32 v[130:131], v[120:121], v[130:131] op_sel_hi:[0,1]
	v_pk_mul_f32 v[148:149], v[120:121], v[148:149] op_sel_hi:[0,1]
	v_pk_mul_f32 v[132:133], v[120:121], v[132:133] op_sel_hi:[0,1]
	s_waitcnt vmcnt(3)
	v_lshlrev_b32_e32 v145, 16, v135
	v_lshlrev_b32_e32 v144, 16, v134
	v_and_b32_e32 v135, 0xffff0000, v135
	v_and_b32_e32 v134, 0xffff0000, v134
	v_lshlrev_b32_e32 v151, 16, v137
	v_lshlrev_b32_e32 v150, 16, v136
	v_and_b32_e32 v137, 0xffff0000, v137
	v_and_b32_e32 v136, 0xffff0000, v136
	v_pk_fma_f32 v[140:141], v[122:123], v[140:141], v[142:143] op_sel_hi:[0,1,1]
	v_pk_fma_f32 v[126:127], v[122:123], v[126:127], v[130:131] op_sel_hi:[0,1,1]
	v_pk_fma_f32 v[130:131], v[122:123], v[146:147], v[148:149] op_sel_hi:[0,1,1]
	v_pk_fma_f32 v[128:129], v[122:123], v[128:129], v[132:133] op_sel_hi:[0,1,1]
	v_pk_fma_f32 v[132:133], v[152:153], v[144:145], v[140:141] op_sel_hi:[0,1,1]
	v_pk_fma_f32 v[126:127], v[152:153], v[134:135], v[126:127] op_sel_hi:[0,1,1]
	v_pk_fma_f32 v[130:131], v[152:153], v[150:151], v[130:131] op_sel_hi:[0,1,1]
	v_pk_fma_f32 v[128:129], v[152:153], v[136:137], v[128:129] op_sel_hi:[0,1,1]
	v_bfe_u32 v120, v129, 16, 1
	v_bfe_u32 v122, v128, 16, 1
	v_bfe_u32 v125, v127, 16, 1
	v_bfe_u32 v135, v132, 16, 1
	v_bfe_u32 v136, v133, 16, 1
	v_bfe_u32 v137, v130, 16, 1
	v_bfe_u32 v140, v131, 16, 1
	v_bfe_u32 v134, v126, 16, 1
	v_add3_u32 v125, v127, v125, s22
	v_add3_u32 v122, v128, v122, s22
	v_add3_u32 v120, v129, v120, s22
	v_add3_u32 v127, v131, v140, s22
	v_add3_u32 v128, v130, v137, s22
	v_add3_u32 v129, v133, v136, s22
	v_add3_u32 v130, v132, v135, s22
	v_add3_u32 v126, v126, v134, s22
	v_lshrrev_b32_e32 v130, 16, v130
	v_lshrrev_b32_e32 v131, 16, v129
	v_lshrrev_b32_e32 v128, 16, v128
	v_lshrrev_b32_e32 v127, 16, v127
	v_and_or_b32 v129, v120, s21, v127
	v_and_or_b32 v128, v122, s21, v128
	v_and_or_b32 v127, v125, s21, v131
	v_and_or_b32 v126, v126, s21, v130
	global_store_dwordx4 v[138:139], v[126:129], off
	s_andn2_b64 exec, exec, s[14:15]
	s_cbranch_execnz .LBB0_1060

.LBB0_1318:
	s_waitcnt vmcnt(4)
	v_mov_b64_e32 v[128:129], v[4:5]
	v_mov_b64_e32 v[124:125], v[8:9]
	v_mov_b64_e32 v[120:121], v[12:13]
	v_mov_b64_e32 v[112:113], v[16:17]
	v_mov_b64_e32 v[108:109], v[20:21]
	v_mov_b64_e32 v[104:105], v[24:25]
	v_mov_b64_e32 v[100:101], v[28:29]
	v_mov_b64_e32 v[96:97], v[32:33]
	v_mov_b64_e32 v[92:93], v[36:37]
	v_mov_b64_e32 v[88:89], v[40:41]
	v_mov_b64_e32 v[84:85], v[44:45]
	v_mov_b64_e32 v[72:73], v[52:53]
	v_mov_b64_e32 v[68:69], v[60:61]
	v_mov_b64_e32 v[54:55], v[62:63]
	v_mov_b64_e32 v[46:47], v[74:75]
	v_mov_b64_e32 v[116:117], v[80:81]
	v_add_u32_e32 v143, s25, v143
	s_add_i32 s26, s26, s27
	s_add_i32 s28, s28, s25
	s_add_i32 s29, s29, s30
	s_andn2_b64 vcc, exec, s[12:13]
	s_mov_b32 s34, s31
	v_mov_b64_e32 v[126:127], v[2:3]
	v_mov_b64_e32 v[122:123], v[6:7]
	v_mov_b64_e32 v[118:119], v[10:11]
	v_mov_b64_e32 v[110:111], v[14:15]
	v_mov_b64_e32 v[106:107], v[18:19]
	v_mov_b64_e32 v[102:103], v[22:23]
	v_mov_b64_e32 v[98:99], v[26:27]
	v_mov_b64_e32 v[94:95], v[30:31]
	v_mov_b64_e32 v[90:91], v[34:35]
	v_mov_b64_e32 v[86:87], v[38:39]
	v_mov_b64_e32 v[82:83], v[42:43]
	v_mov_b64_e32 v[70:71], v[50:51]
	v_mov_b64_e32 v[66:67], v[58:59]
	v_mov_b64_e32 v[56:57], v[64:65]
	v_mov_b64_e32 v[48:49], v[76:77]
	v_mov_b64_e32 v[114:115], v[78:79]
	s_cbranch_vccz .LBB0_1329

.LBB0_1325:
	s_mov_b64 s[14:15], -1
	s_cmp_gt_i32 s33, 0xffff
	v_add_u32_e32 v149, 0x410, v1
	v_add_u32_e32 v150, 0x418, v1
	v_add_u32_e32 v151, 0x820, v1
	v_add_u32_e32 v152, 0x828, v1
	v_add_u32_e32 v153, 0xc30, v1
	v_add_u32_e32 v154, 0xc38, v1
	v_add_u32_e32 v155, 0x1040, v1
	v_add_u32_e32 v156, 0x1048, v1
	v_add_u32_e32 v157, 0x1450, v1
	v_add_u32_e32 v158, 0x1458, v1
	v_add_u32_e32 v159, 0x1860, v1
	v_add_u32_e32 v160, 0x1868, v1
	v_add_u32_e32 v161, 0x1c70, v1
	v_add_u32_e32 v162, 0x1c78, v1
	v_add_u32_e32 v163, 0x2080, v1
	v_add_u32_e32 v164, 0x2088, v1
	v_add_u32_e32 v165, 0x2490, v1
	v_add_u32_e32 v166, 0x2498, v1
	v_add_u32_e32 v167, 0x28a0, v1
	v_add_u32_e32 v168, 0x28a8, v1
	v_add_u32_e32 v169, 0x2cb0, v1
	v_add_u32_e32 v170, 0x2cb8, v1
	v_add_u32_e32 v171, 0x30c0, v1
	v_add_u32_e32 v172, 0x30c8, v1
	v_add_u32_e32 v173, 0x34d0, v1
	v_add_u32_e32 v174, 0x34d8, v1
	v_add_u32_e32 v175, 0x38e0, v1
	v_add_u32_e32 v176, 0x38e8, v1
	v_add_u32_e32 v177, 0x3cf0, v1
	v_add_u32_e32 v178, 0x3cf8, v1
	v_add_u32_e32 v148, 0x400, v145
	v_add_u32_e32 v147, 0x800, v145
	v_add_u32_e32 v146, 0xc00, v145
	s_cbranch_scc0 .LBB0_1327
	s_waitcnt vmcnt(16)
	ds_write2_b32 v1, v126, v127 offset1:1
	ds_write2_b32 v1, v128, v129 offset0:2 offset1:3
	ds_write2_b32 v149, v122, v123 offset1:1
	ds_write2_b32 v150, v124, v125 offset1:1
	ds_write2_b32 v151, v118, v119 offset1:1
	ds_write2_b32 v152, v120, v121 offset1:1
	ds_write2_b32 v153, v110, v111 offset1:1
	ds_write2_b32 v154, v112, v113 offset1:1
	ds_write2_b32 v155, v106, v107 offset1:1
	ds_write2_b32 v156, v108, v109 offset1:1
	ds_write2_b32 v157, v102, v103 offset1:1
	ds_write2_b32 v158, v104, v105 offset1:1
	ds_write2_b32 v159, v98, v99 offset1:1
	ds_write2_b32 v160, v100, v101 offset1:1
	ds_write2_b32 v161, v94, v95 offset1:1
	ds_write2_b32 v162, v96, v97 offset1:1
	ds_write2_b32 v163, v90, v91 offset1:1
	ds_write2_b32 v164, v92, v93 offset1:1
	ds_write2_b32 v165, v86, v87 offset1:1
	ds_write2_b32 v166, v88, v89 offset1:1
	ds_write2_b32 v167, v82, v83 offset1:1
	ds_write2_b32 v168, v84, v85 offset1:1
	ds_write2_b32 v169, v70, v71 offset1:1
	ds_write2_b32 v170, v72, v73 offset1:1
	ds_write2_b32 v171, v66, v67 offset1:1
	ds_write2_b32 v172, v68, v69 offset1:1
	ds_write2_b32 v173, v54, v55 offset1:1
	ds_write2_b32 v174, v56, v57 offset1:1
	ds_write2_b32 v175, v46, v47 offset1:1
	ds_write2_b32 v176, v48, v49 offset1:1
	ds_write2_b32 v177, v114, v115 offset1:1
	ds_write2_b32 v178, v116, v117 offset1:1
	s_waitcnt lgkmcnt(0)
	ds_read2_b32 v[184:185], v145 offset1:16
	ds_read2_b32 v[186:187], v145 offset0:65 offset1:81
	ds_read2_b32 v[188:189], v145 offset0:130 offset1:146
	ds_read2_b32 v[190:191], v145 offset0:195 offset1:211
	v_mov_b32_e32 v180, v131
	s_waitcnt lgkmcnt(0)
	v_mul_f32_e32 v0, 0x43800000, v184
	v_mul_f32_e32 v179, 0x43800000, v186
	ds_read2_b32 v[192:193], v148 offset0:4 offset1:20
	ds_read2_b32 v[194:195], v148 offset0:69 offset1:85
	v_cvt_pk_fp8_f32 v180, v0, v179
	v_mul_f32_e32 v181, 0x43800000, v188
	v_mul_f32_e32 v0, 0x43800000, v190
	ds_read2_b32 v[196:197], v148 offset0:134 offset1:150
	ds_read2_b32 v[198:199], v148 offset0:199 offset1:215
	v_cvt_pk_fp8_f32 v180, v181, v0 op_sel:[0,0,1]
	s_waitcnt lgkmcnt(3)
	v_mul_f32_e32 v0, 0x43800000, v192
	s_waitcnt lgkmcnt(2)
	v_mul_f32_e32 v179, 0x43800000, v194
	v_mov_b32_e32 v181, v131
	ds_read2_b32 v[200:201], v147 offset0:8 offset1:24
	v_cvt_pk_fp8_f32 v181, v0, v179
	ds_read2_b32 v[202:203], v147 offset0:73 offset1:89
	ds_read2_b32 v[204:205], v147 offset0:138 offset1:154
	ds_read2_b32 v[206:207], v147 offset0:203 offset1:219
	ds_read2_b32 v[208:209], v146 offset0:12 offset1:28
	ds_read2_b32 v[210:211], v146 offset0:77 offset1:93
	s_lshr_b32 s10, s34, 10
	s_waitcnt lgkmcnt(7)
	v_mul_f32_e32 v182, 0x43800000, v196
	s_waitcnt lgkmcnt(6)
	v_mul_f32_e32 v0, 0x43800000, v198
	s_lshl_b64 s[0:1], s[10:11], 22
	v_cvt_pk_fp8_f32 v181, v182, v0 op_sel:[0,0,1]
	s_waitcnt lgkmcnt(5)
	v_mul_f32_e32 v0, 0x43800000, v200
	s_waitcnt lgkmcnt(4)
	v_mul_f32_e32 v179, 0x43800000, v202
	v_mov_b32_e32 v182, v131
	ds_read2_b32 v[212:213], v146 offset0:142 offset1:158
	ds_read2_b32 v[214:215], v146 offset0:207 offset1:223
	s_add_u32 s0, s22, s0
	v_cvt_pk_fp8_f32 v182, v0, v179
	s_waitcnt lgkmcnt(3)
	v_mul_f32_e32 v0, 0x43800000, v208
	s_waitcnt lgkmcnt(2)
	v_mul_f32_e32 v179, 0x43800000, v210
	v_mov_b32_e32 v183, v131
	s_addc_u32 s1, s23, s1
	s_and_b32 s2, s26, 0x1f0
	s_bfe_u32 s3, s33, 0x40006
	v_cvt_pk_fp8_f32 v183, v0, v179
	s_or_b32 s2, s2, s3
	s_lshl_b32 s2, s2, 13
	s_add_u32 s0, s0, s2
	v_mul_f32_e32 v184, 0x43800000, v204
	v_mul_f32_e32 v186, 0x43800000, v206
	s_waitcnt lgkmcnt(1)
	v_mul_f32_e32 v0, 0x43800000, v212
	s_waitcnt lgkmcnt(0)
	v_mul_f32_e32 v179, 0x43800000, v214
	s_addc_u32 s1, s1, 0
	v_and_b32_e32 v130, 64, v143
	v_cvt_pk_fp8_f32 v182, v184, v186 op_sel:[0,0,1]
	v_cvt_pk_fp8_f32 v183, v0, v179 op_sel:[0,0,1]
	v_lshl_add_u64 v[216:217], s[0:1], 0, v[130:131]
	v_lshl_add_u64 v[216:217], v[216:217], 0, v[132:133]
	v_lshl_add_u64 v[218:219], v[216:217], 0, v[134:135]
	global_store_dwordx4 v[218:219], v[180:183], off nt
	v_mul_f32_e32 v0, 0x43800000, v185
	v_mul_f32_e32 v130, 0x43800000, v187
	v_mov_b32_e32 v180, v131
	v_cvt_pk_fp8_f32 v180, v0, v130
	v_mul_f32_e32 v0, 0x43800000, v193
	v_mul_f32_e32 v130, 0x43800000, v195
	v_mov_b32_e32 v181, v131
	v_cvt_pk_fp8_f32 v181, v0, v130
	v_mul_f32_e32 v179, 0x43800000, v189
	v_mul_f32_e32 v182, 0x43800000, v191
	v_mul_f32_e32 v0, 0x43800000, v197
	v_mul_f32_e32 v130, 0x43800000, v199
	v_cvt_pk_fp8_f32 v180, v179, v182 op_sel:[0,0,1]
	v_cvt_pk_fp8_f32 v181, v0, v130 op_sel:[0,0,1]
	v_mul_f32_e32 v0, 0x43800000, v201
	v_mul_f32_e32 v130, 0x43800000, v203
	v_mov_b32_e32 v182, v131
	v_cvt_pk_fp8_f32 v182, v0, v130
	v_mul_f32_e32 v0, 0x43800000, v209
	v_mul_f32_e32 v130, 0x43800000, v211
	v_mov_b32_e32 v183, v131
	v_cvt_pk_fp8_f32 v183, v0, v130
	v_mul_f32_e32 v179, 0x43800000, v205
	v_mul_f32_e32 v184, 0x43800000, v207
	v_mul_f32_e32 v0, 0x43800000, v213
	v_mul_f32_e32 v130, 0x43800000, v215
	v_cvt_pk_fp8_f32 v182, v179, v184 op_sel:[0,0,1]
	v_cvt_pk_fp8_f32 v183, v0, v130 op_sel:[0,0,1]
	ds_read2_b32 v[184:185], v145 offset0:32 offset1:48
	ds_read2_b32 v[186:187], v145 offset0:97 offset1:113
	ds_read2_b32 v[188:189], v145 offset0:162 offset1:178
	v_lshl_add_u64 v[190:191], v[216:217], 0, v[136:137]
	s_mov_b64 s[14:15], 0
	global_store_dwordx4 v[190:191], v[180:183], off nt
	ds_read2_b32 v[190:191], v145 offset0:227 offset1:243
	s_waitcnt lgkmcnt(3)
	v_mul_f32_e32 v0, 0x43800000, v184
	s_waitcnt lgkmcnt(2)
	v_mul_f32_e32 v130, 0x43800000, v186
	v_mov_b32_e32 v180, v131
	ds_read2_b32 v[192:193], v148 offset0:36 offset1:52
	ds_read2_b32 v[194:195], v148 offset0:101 offset1:117
	v_cvt_pk_fp8_f32 v180, v0, v130
	s_waitcnt lgkmcnt(3)
	v_mul_f32_e32 v179, 0x43800000, v188
	s_waitcnt lgkmcnt(2)
	v_mul_f32_e32 v0, 0x43800000, v190
	ds_read2_b32 v[196:197], v148 offset0:166 offset1:182
	ds_read2_b32 v[198:199], v148 offset0:231 offset1:247
	v_cvt_pk_fp8_f32 v180, v179, v0 op_sel:[0,0,1]
	s_waitcnt lgkmcnt(3)
	v_mul_f32_e32 v0, 0x43800000, v192
	s_waitcnt lgkmcnt(2)
	v_mul_f32_e32 v130, 0x43800000, v194
	v_mov_b32_e32 v181, v131
	ds_read2_b32 v[200:201], v147 offset0:40 offset1:56
	v_cvt_pk_fp8_f32 v181, v0, v130
	ds_read2_b32 v[202:203], v147 offset0:105 offset1:121
	ds_read2_b32 v[204:205], v147 offset0:170 offset1:186
	ds_read2_b32 v[206:207], v147 offset0:235 offset1:251
	ds_read2_b32 v[208:209], v146 offset0:44 offset1:60
	ds_read2_b32 v[210:211], v146 offset0:109 offset1:125
	s_waitcnt lgkmcnt(7)
	v_mul_f32_e32 v179, 0x43800000, v196
	s_waitcnt lgkmcnt(6)
	v_mul_f32_e32 v0, 0x43800000, v198
	v_cvt_pk_fp8_f32 v181, v179, v0 op_sel:[0,0,1]
	s_waitcnt lgkmcnt(5)
	v_mul_f32_e32 v0, 0x43800000, v200
	s_waitcnt lgkmcnt(4)
	v_mul_f32_e32 v130, 0x43800000, v202
	v_mov_b32_e32 v182, v131
	ds_read2_b32 v[212:213], v146 offset0:174 offset1:190
	ds_read2_b32 v[214:215], v146 offset0:239 offset1:255
	v_cvt_pk_fp8_f32 v182, v0, v130
	s_waitcnt lgkmcnt(3)
	v_mul_f32_e32 v0, 0x43800000, v208
	s_waitcnt lgkmcnt(2)
	v_mul_f32_e32 v130, 0x43800000, v210
	v_mov_b32_e32 v183, v131
	v_cvt_pk_fp8_f32 v183, v0, v130
	v_mul_f32_e32 v179, 0x43800000, v204
	v_mul_f32_e32 v184, 0x43800000, v206
	s_waitcnt lgkmcnt(1)
	v_mul_f32_e32 v0, 0x43800000, v212
	s_waitcnt lgkmcnt(0)
	v_mul_f32_e32 v130, 0x43800000, v214
	v_cvt_pk_fp8_f32 v182, v179, v184 op_sel:[0,0,1]
	v_cvt_pk_fp8_f32 v183, v0, v130 op_sel:[0,0,1]
	v_mul_f32_e32 v0, 0x43800000, v185
	v_mul_f32_e32 v130, 0x43800000, v187
	v_mov_b32_e32 v184, v131
	v_cvt_pk_fp8_f32 v184, v0, v130
	v_mul_f32_e32 v0, 0x43800000, v193
	v_mul_f32_e32 v130, 0x43800000, v195
	v_mov_b32_e32 v185, v131
	v_cvt_pk_fp8_f32 v185, v0, v130
	v_mul_f32_e32 v179, 0x43800000, v189
	v_mul_f32_e32 v186, 0x43800000, v191
	v_mul_f32_e32 v0, 0x43800000, v197
	v_mul_f32_e32 v130, 0x43800000, v199
	v_cvt_pk_fp8_f32 v184, v179, v186 op_sel:[0,0,1]
	v_cvt_pk_fp8_f32 v185, v0, v130 op_sel:[0,0,1]
	v_mul_f32_e32 v0, 0x43800000, v201
	v_mul_f32_e32 v130, 0x43800000, v203
	v_mov_b32_e32 v186, v131
	v_cvt_pk_fp8_f32 v186, v0, v130
	v_mul_f32_e32 v0, 0x43800000, v209
	v_mul_f32_e32 v130, 0x43800000, v211
	v_mov_b32_e32 v187, v131
	v_cvt_pk_fp8_f32 v187, v0, v130
	v_mul_f32_e32 v179, 0x43800000, v205
	v_mul_f32_e32 v188, 0x43800000, v207
	v_mul_f32_e32 v0, 0x43800000, v213
	v_mul_f32_e32 v130, 0x43800000, v215
	v_cvt_pk_fp8_f32 v186, v179, v188 op_sel:[0,0,1]
	v_cvt_pk_fp8_f32 v187, v0, v130 op_sel:[0,0,1]
	v_lshl_add_u64 v[188:189], v[216:217], 0, v[138:139]
	global_store_dwordx4 v[188:189], v[180:183], off nt
	s_nop 1
	v_lshl_add_u64 v[180:181], v[216:217], 0, v[140:141]
	global_store_dwordx4 v[180:181], v[184:187], off nt
	s_waitcnt lgkmcnt(0)
.LBB0_1327:
	s_andn2_b64 vcc, exec, s[14:15]
	s_cbranch_vccnz .LBB0_1318
	s_waitcnt vmcnt(16)
	ds_write2_b32 v1, v126, v127 offset1:1
	ds_write2_b32 v1, v128, v129 offset0:2 offset1:3
	ds_write2_b32 v149, v122, v123 offset1:1
	ds_write2_b32 v150, v124, v125 offset1:1
	ds_write2_b32 v151, v118, v119 offset1:1
	ds_write2_b32 v152, v120, v121 offset1:1
	ds_write2_b32 v153, v110, v111 offset1:1
	ds_write2_b32 v154, v112, v113 offset1:1
	ds_write2_b32 v155, v106, v107 offset1:1
	ds_write2_b32 v156, v108, v109 offset1:1
	ds_write2_b32 v157, v102, v103 offset1:1
	ds_write2_b32 v158, v104, v105 offset1:1
	ds_write2_b32 v159, v98, v99 offset1:1
	ds_write2_b32 v160, v100, v101 offset1:1
	ds_write2_b32 v161, v94, v95 offset1:1
	ds_write2_b32 v162, v96, v97 offset1:1
	ds_write2_b32 v163, v90, v91 offset1:1
	ds_write2_b32 v164, v92, v93 offset1:1
	ds_write2_b32 v165, v86, v87 offset1:1
	ds_write2_b32 v166, v88, v89 offset1:1
	ds_write2_b32 v167, v82, v83 offset1:1
	ds_write2_b32 v168, v84, v85 offset1:1
	ds_write2_b32 v169, v70, v71 offset1:1
	ds_write2_b32 v170, v72, v73 offset1:1
	ds_write2_b32 v171, v66, v67 offset1:1
	ds_write2_b32 v172, v68, v69 offset1:1
	ds_write2_b32 v173, v54, v55 offset1:1
	ds_write2_b32 v174, v56, v57 offset1:1
	ds_write2_b32 v175, v46, v47 offset1:1
	ds_write2_b32 v176, v48, v49 offset1:1
	ds_write2_b32 v177, v114, v115 offset1:1
	ds_write2_b32 v178, v116, v117 offset1:1
	s_waitcnt lgkmcnt(0)
	ds_read2_b32 v[54:55], v145 offset1:16
	ds_read2_b32 v[56:57], v145 offset0:65 offset1:81
	ds_read2_b32 v[66:67], v145 offset0:130 offset1:146
	ds_read2_b32 v[68:69], v145 offset0:195 offset1:211
	v_mov_b32_e32 v46, v131
	s_waitcnt lgkmcnt(0)
	v_mul_f32_e32 v0, 0x43800000, v54
	v_mul_f32_e32 v47, 0x43800000, v56
	ds_read2_b32 v[70:71], v148 offset0:4 offset1:20
	ds_read2_b32 v[72:73], v148 offset0:69 offset1:85
	v_cvt_pk_fp8_f32 v46, v0, v47
	v_mul_f32_e32 v48, 0x43800000, v66
	v_mul_f32_e32 v0, 0x43800000, v68
	ds_read2_b32 v[82:83], v148 offset0:134 offset1:150
	ds_read2_b32 v[84:85], v148 offset0:199 offset1:215
	v_cvt_pk_fp8_f32 v46, v48, v0 op_sel:[0,0,1]
	s_waitcnt lgkmcnt(3)
	v_mul_f32_e32 v0, 0x43800000, v70
	s_waitcnt lgkmcnt(2)
	v_mul_f32_e32 v48, 0x43800000, v72
	v_mov_b32_e32 v47, v131
	ds_read2_b32 v[86:87], v147 offset0:8 offset1:24
	v_cvt_pk_fp8_f32 v47, v0, v48
	ds_read2_b32 v[88:89], v147 offset0:73 offset1:89
	ds_read2_b32 v[90:91], v147 offset0:138 offset1:154
	ds_read2_b32 v[92:93], v147 offset0:203 offset1:219
	ds_read2_b32 v[94:95], v146 offset0:12 offset1:28
	ds_read2_b32 v[96:97], v146 offset0:77 offset1:93
	s_ashr_i32 s0, s33, 11
	s_ashr_i32 s1, s0, 31
	s_lshl_b64 s[0:1], s[0:1], 23
	s_waitcnt lgkmcnt(7)
	v_mul_f32_e32 v49, 0x43800000, v82
	s_waitcnt lgkmcnt(6)
	v_mul_f32_e32 v0, 0x43800000, v84
	s_add_u32 s0, s20, s0
	v_cvt_pk_fp8_f32 v47, v49, v0 op_sel:[0,0,1]
	s_waitcnt lgkmcnt(5)
	v_mul_f32_e32 v0, 0x43800000, v86
	s_waitcnt lgkmcnt(4)
	v_mul_f32_e32 v49, 0x43800000, v88
	v_mov_b32_e32 v48, v131
	ds_read2_b32 v[98:99], v146 offset0:142 offset1:158
	ds_read2_b32 v[100:101], v146 offset0:207 offset1:223
	s_addc_u32 s1, s21, s1
	s_and_b32 s2, s26, 0x3f0
	s_bfe_u32 s3, s33, 0x40007
	v_cvt_pk_fp8_f32 v48, v0, v49
	s_waitcnt lgkmcnt(3)
	v_mul_f32_e32 v0, 0x43800000, v94
	s_waitcnt lgkmcnt(2)
	v_mul_f32_e32 v66, 0x43800000, v96
	v_mov_b32_e32 v49, v131
	s_or_b32 s2, s2, s3
	v_cvt_pk_fp8_f32 v49, v0, v66
	s_lshl_b32 s2, s2, 13
	s_add_u32 s0, s0, s2
	v_mul_f32_e32 v54, 0x43800000, v90
	v_mul_f32_e32 v56, 0x43800000, v92
	s_addc_u32 s1, s1, 0
	s_and_b32 s2, s33, 64
	v_cvt_pk_fp8_f32 v48, v54, v56 op_sel:[0,0,1]
	s_waitcnt lgkmcnt(1)
	v_mul_f32_e32 v0, 0x43800000, v98
	s_waitcnt lgkmcnt(0)
	v_mul_f32_e32 v54, 0x43800000, v100
	s_add_u32 s0, s0, s2
	v_cvt_pk_fp8_f32 v49, v0, v54 op_sel:[0,0,1]
	s_addc_u32 s1, s1, 0
	v_lshl_add_u64 v[102:103], s[0:1], 0, v[132:133]
	v_lshl_add_u64 v[104:105], v[102:103], 0, v[134:135]
	global_store_dwordx4 v[104:105], v[46:49], off nt
	v_mul_f32_e32 v0, 0x43800000, v55
	v_mul_f32_e32 v54, 0x43800000, v73
	v_mul_f32_e32 v47, 0x43800000, v57
	v_mov_b32_e32 v46, v131
	v_cvt_pk_fp8_f32 v46, v0, v47
	v_mul_f32_e32 v0, 0x43800000, v71
	v_mov_b32_e32 v47, v131
	v_cvt_pk_fp8_f32 v47, v0, v54
	v_mul_f32_e32 v48, 0x43800000, v67
	v_mul_f32_e32 v49, 0x43800000, v69
	v_cvt_pk_fp8_f32 v46, v48, v49 op_sel:[0,0,1]
	v_mul_f32_e32 v0, 0x43800000, v83
	v_mul_f32_e32 v48, 0x43800000, v85
	v_cvt_pk_fp8_f32 v47, v0, v48 op_sel:[0,0,1]
	v_mul_f32_e32 v0, 0x43800000, v87
	v_mul_f32_e32 v49, 0x43800000, v89
	v_mov_b32_e32 v48, v131
	v_cvt_pk_fp8_f32 v48, v0, v49
	v_mul_f32_e32 v0, 0x43800000, v95
	v_mul_f32_e32 v56, 0x43800000, v97
	v_mov_b32_e32 v49, v131
	v_cvt_pk_fp8_f32 v49, v0, v56
	v_mul_f32_e32 v54, 0x43800000, v91
	v_mul_f32_e32 v55, 0x43800000, v93
	v_cvt_pk_fp8_f32 v48, v54, v55 op_sel:[0,0,1]
	v_mul_f32_e32 v0, 0x43800000, v99
	v_mul_f32_e32 v54, 0x43800000, v101
	v_cvt_pk_fp8_f32 v49, v0, v54 op_sel:[0,0,1]
	ds_read2_b32 v[54:55], v145 offset0:32 offset1:48
	ds_read2_b32 v[56:57], v145 offset0:97 offset1:113
	ds_read2_b32 v[66:67], v145 offset0:162 offset1:178
	v_lshl_add_u64 v[68:69], v[102:103], 0, v[136:137]
	global_store_dwordx4 v[68:69], v[46:49], off nt
	ds_read2_b32 v[68:69], v145 offset0:227 offset1:243
	s_waitcnt lgkmcnt(3)
	v_mul_f32_e32 v0, 0x43800000, v54
	s_waitcnt lgkmcnt(2)
	v_mul_f32_e32 v47, 0x43800000, v56
	v_mov_b32_e32 v46, v131
	ds_read2_b32 v[70:71], v148 offset0:36 offset1:52
	ds_read2_b32 v[72:73], v148 offset0:101 offset1:117
	v_cvt_pk_fp8_f32 v46, v0, v47
	s_waitcnt lgkmcnt(3)
	v_mul_f32_e32 v48, 0x43800000, v66
	s_waitcnt lgkmcnt(2)
	v_mul_f32_e32 v0, 0x43800000, v68
	ds_read2_b32 v[82:83], v148 offset0:166 offset1:182
	ds_read2_b32 v[84:85], v148 offset0:231 offset1:247
	v_cvt_pk_fp8_f32 v46, v48, v0 op_sel:[0,0,1]
	s_waitcnt lgkmcnt(3)
	v_mul_f32_e32 v0, 0x43800000, v70
	s_waitcnt lgkmcnt(2)
	v_mul_f32_e32 v48, 0x43800000, v72
	v_mov_b32_e32 v47, v131
	ds_read2_b32 v[86:87], v147 offset0:40 offset1:56
	v_cvt_pk_fp8_f32 v47, v0, v48
	ds_read2_b32 v[88:89], v147 offset0:105 offset1:121
	ds_read2_b32 v[90:91], v147 offset0:170 offset1:186
	ds_read2_b32 v[92:93], v147 offset0:235 offset1:251
	ds_read2_b32 v[94:95], v146 offset0:44 offset1:60
	ds_read2_b32 v[96:97], v146 offset0:109 offset1:125
	s_waitcnt lgkmcnt(7)
	v_mul_f32_e32 v49, 0x43800000, v82
	s_waitcnt lgkmcnt(6)
	v_mul_f32_e32 v0, 0x43800000, v84
	v_cvt_pk_fp8_f32 v47, v49, v0 op_sel:[0,0,1]
	s_waitcnt lgkmcnt(5)
	v_mul_f32_e32 v0, 0x43800000, v86
	s_waitcnt lgkmcnt(4)
	v_mul_f32_e32 v49, 0x43800000, v88
	v_mov_b32_e32 v48, v131
	ds_read2_b32 v[98:99], v146 offset0:174 offset1:190
	ds_read2_b32 v[100:101], v146 offset0:239 offset1:255
	v_cvt_pk_fp8_f32 v48, v0, v49
	s_waitcnt lgkmcnt(3)
	v_mul_f32_e32 v0, 0x43800000, v94
	s_waitcnt lgkmcnt(2)
	v_mul_f32_e32 v66, 0x43800000, v96
	v_mov_b32_e32 v49, v131
	v_cvt_pk_fp8_f32 v49, v0, v66
	v_mul_f32_e32 v54, 0x43800000, v90
	v_mul_f32_e32 v56, 0x43800000, v92
	v_cvt_pk_fp8_f32 v48, v54, v56 op_sel:[0,0,1]
	s_waitcnt lgkmcnt(1)
	v_mul_f32_e32 v0, 0x43800000, v98
	s_waitcnt lgkmcnt(0)
	v_mul_f32_e32 v54, 0x43800000, v100
	v_cvt_pk_fp8_f32 v49, v0, v54 op_sel:[0,0,1]
	v_mul_f32_e32 v0, 0x43800000, v55
	v_mul_f32_e32 v55, 0x43800000, v57
	v_mov_b32_e32 v54, v131
	v_cvt_pk_fp8_f32 v54, v0, v55
	v_mul_f32_e32 v0, 0x43800000, v71
	v_mul_f32_e32 v66, 0x43800000, v73
	v_mov_b32_e32 v55, v131
	v_cvt_pk_fp8_f32 v55, v0, v66
	v_mul_f32_e32 v56, 0x43800000, v67
	v_mul_f32_e32 v57, 0x43800000, v69
	v_cvt_pk_fp8_f32 v54, v56, v57 op_sel:[0,0,1]
	v_mul_f32_e32 v0, 0x43800000, v83
	v_mul_f32_e32 v56, 0x43800000, v85
	v_cvt_pk_fp8_f32 v55, v0, v56 op_sel:[0,0,1]
	v_mul_f32_e32 v0, 0x43800000, v87
	v_mul_f32_e32 v57, 0x43800000, v89
	v_mov_b32_e32 v56, v131
	v_cvt_pk_fp8_f32 v56, v0, v57
	v_mul_f32_e32 v0, 0x43800000, v95
	v_mul_f32_e32 v68, 0x43800000, v97
	v_mov_b32_e32 v57, v131
	v_cvt_pk_fp8_f32 v57, v0, v68
	v_mul_f32_e32 v66, 0x43800000, v91
	v_mul_f32_e32 v67, 0x43800000, v93
	v_cvt_pk_fp8_f32 v56, v66, v67 op_sel:[0,0,1]
	v_mul_f32_e32 v0, 0x43800000, v99
	v_mul_f32_e32 v66, 0x43800000, v101
	v_cvt_pk_fp8_f32 v57, v0, v66 op_sel:[0,0,1]
	v_lshl_add_u64 v[66:67], v[102:103], 0, v[138:139]
	global_store_dwordx4 v[66:67], v[46:49], off nt
	s_nop 1
	v_lshl_add_u64 v[46:47], v[102:103], 0, v[140:141]
	global_store_dwordx4 v[46:47], v[54:57], off nt
	s_waitcnt lgkmcnt(0)
	s_branch .LBB0_1318

	.amdhsa_kernel _Z3fwd4Args
		.amdhsa_group_segment_fixed_size 0
		.amdhsa_private_segment_fixed_size 0
		.amdhsa_kernarg_size 504
		.amdhsa_user_sgpr_count 2
		.amdhsa_user_sgpr_dispatch_ptr 0
		.amdhsa_user_sgpr_queue_ptr 0
		.amdhsa_user_sgpr_kernarg_segment_ptr 1
		.amdhsa_user_sgpr_dispatch_id 0
		.amdhsa_user_sgpr_kernarg_preload_length 0
		.amdhsa_user_sgpr_kernarg_preload_offset 0
		.amdhsa_user_sgpr_private_segment_size 0
		.amdhsa_uses_dynamic_stack 0
		.amdhsa_enable_private_segment 0
		.amdhsa_system_sgpr_workgroup_id_x 1
		.amdhsa_system_sgpr_workgroup_id_y 0
		.amdhsa_system_sgpr_workgroup_id_z 0
		.amdhsa_system_sgpr_workgroup_info 0
		.amdhsa_system_vgpr_workitem_id 0
		.amdhsa_next_free_vgpr 256
		.amdhsa_next_free_sgpr 102
		.amdhsa_accum_offset 256
		.amdhsa_reserve_vcc 1
		.amdhsa_float_round_mode_32 0
		.amdhsa_float_round_mode_16_64 0
		.amdhsa_float_denorm_mode_32 3
		.amdhsa_float_denorm_mode_16_64 3
		.amdhsa_dx10_clamp 1
		.amdhsa_ieee_mode 1
		.amdhsa_fp16_overflow 0
		.amdhsa_tg_split 0
		.amdhsa_exception_fp_ieee_invalid_op 0
		.amdhsa_exception_fp_denorm_src 0
		.amdhsa_exception_fp_ieee_div_zero 0
		.amdhsa_exception_fp_ieee_overflow 0
		.amdhsa_exception_fp_ieee_underflow 0
		.amdhsa_exception_fp_ieee_inexact 0
		.amdhsa_exception_int_div_zero 0
	.end_amdhsa_kernel

amdhsa.kernels:
  - .agpr_count:     0
    .args:
      - .offset:         0
        .size:           248
        .value_kind:     by_value
      - .offset:         248
        .size:           4
        .value_kind:     hidden_block_count_x
      - .offset:         252
        .size:           4
        .value_kind:     hidden_block_count_y
      - .offset:         256
        .size:           4
        .value_kind:     hidden_block_count_z
      - .offset:         260
        .size:           2
        .value_kind:     hidden_group_size_x
      - .offset:         262
        .size:           2
        .value_kind:     hidden_group_size_y
      - .offset:         264
        .size:           2
        .value_kind:     hidden_group_size_z
      - .offset:         266
        .size:           2
        .value_kind:     hidden_remainder_x
      - .offset:         268
        .size:           2
        .value_kind:     hidden_remainder_y
      - .offset:         270
        .size:           2
        .value_kind:     hidden_remainder_z
      - .offset:         288
        .size:           8
        .value_kind:     hidden_global_offset_x
      - .offset:         296
        .size:           8
        .value_kind:     hidden_global_offset_y
      - .offset:         304
        .size:           8
        .value_kind:     hidden_global_offset_z
      - .offset:         312
        .size:           2
        .value_kind:     hidden_grid_dims
      - .offset:         368
        .size:           4
        .value_kind:     hidden_dynamic_lds_size
    .group_segment_fixed_size: 0
    .kernarg_segment_align: 8
    .kernarg_segment_size: 504
    .language:       OpenCL C
    .language_version:
      - 2
      - 0
    .max_flat_workgroup_size: 512
    .name:           _Z3fwd4Args
    .private_segment_fixed_size: 0
    .sgpr_count:     108
    .sgpr_spill_count: 62
    .symbol:         _Z3fwd4Args.kd
    .uniform_work_group_size: 1
    .uses_dynamic_stack: false
    .vgpr_count:     256
    .vgpr_spill_count: 0
    .wavefront_size: 64
